# baseline (speedup 1.0000x reference)
_Z16closed_form_mainPKfS0_PKiPf:
	s_load_dwordx8 s[16:23], s[0:1], 0x0
	s_lshr_b32 s6, s2, 3
	v_readfirstlane_b32 s0, v0
	s_mul_hi_u32 s7, s6, 0x24924925
	s_lshr_b32 s4, s0, 6
	s_and_b32 s0, s2, 7
	s_mul_i32 s1, s7, 7
	s_bfe_u32 s5, s2, 0x10003
	s_sub_i32 s1, s6, s1
	s_mul_i32 s36, s0, 7
	s_xor_b32 s3, s4, s5
	s_add_i32 s36, s36, s1
	s_waitcnt lgkmcnt(0)
	s_mov_b64 s[28:29], s[22:23]
	v_and_b32_e32 v19, 63, v0
	s_cmp_lt_u32 s36, 52
	s_mov_b64 s[0:1], -1
	s_cbranch_scc0 .LBB0_32
	s_mul_hi_u32 s0, s6, 0x20820821
	s_lshr_b32 s38, s0, 3
	s_mul_hi_u32 s0, s7, 0x1c71c71d
	s_mul_i32 s0, s0, 9
	s_sub_i32 s0, s7, s0
	v_add_u32_e32 v2, -3, v19
	v_mad_u64_u32 v[0:1], s[0:1], s0, 57, v[2:3]
	s_mov_b64 s[24:25], s[18:19]
	v_mov_b32_e32 v1, 0x200
	v_med3_i32 v1, v0, 0, v1
	s_mul_i32 s34, s36, 10
	s_and_b32 s17, s17, 0xffff
	s_and_b32 s25, s25, 0xffff
	v_cmp_gt_u32_e64 s[0:1], 57, v2
	s_mov_b32 s19, 0x20000
	s_mov_b32 s18, 0xe0e038
	s_mov_b32 s26, 0x606018
	s_mul_i32 s35, s38, 0x70701c
	s_mul_i32 s33, s38, 0x30300c
	v_lshlrev_b32_e32 v28, 2, v1
	v_mul_u32_u24_e32 v27, 12, v1
	v_lshlrev_b32_e32 v23, 4, v19
	s_cmp_lg_u32 s4, s5
	v_sub_u32_e64 v29, s34, 2 clamp
	s_cbranch_scc0 .LBB0_15
	s_setprio 2
	s_mov_b32 s27, s19
	s_and_b32 s21, s21, 0xffff
	s_mov_b32 s22, 0x202008
	s_mov_b32 s23, s19
	s_mul_i32 s38, s38, 0x101004
	s_movk_i32 s37, 0x80
	v_add_u32_e32 v18, -1, v0
	s_movk_i32 s4, 0x201
	s_movk_i32 s5, 0x1ff
	v_cmp_gt_u32_e64 s[40:41], s4, v0
	v_cmp_gt_u32_e64 s[42:43], s5, v18
	v_mov_b32_e32 v18, 0x42c80000
	v_mov_b32_e32 v22, 0x3de38e39
	v_mov_b32_e32 v26, 0x3a3d6628
	v_mov_b32_e32 v1, 0
	s_add_i32 s4, s34, -3
	s_max_i32 s4, s4, 0
	s_mul_i32 s4, s4, 0x804
	s_add_i32 s4, s4, s38
	buffer_load_dword v29, v28, s[20:23], s4 offen nt
	s_add_i32 s4, s34, -2
	s_max_i32 s4, s4, 0
	s_mul_i32 s4, s4, 0x804
	s_add_i32 s4, s4, s38
	buffer_load_dword v2, v28, s[20:23], s4 offen nt
	s_add_i32 s5, s34, -2
	s_max_i32 s5, s5, 0
	s_mul_i32 s6, s5, 0x804
	s_add_i32 s6, s6, s35
	s_add_i32 s7, s6, 0x505014
	s_add_i32 s8, s6, 0x606018
	s_mul_i32 s9, s5, 0x180c
	s_add_i32 s9, s9, s33
	s_add_i32 s4, s34, -1
	s_max_i32 s4, s4, 0
	s_mul_i32 s4, s4, 0x804
	s_add_i32 s4, s4, s38
	buffer_load_dword v3, v28, s[20:23], s4 offen nt
	buffer_load_dwordx3 v[8:10], v27, s[24:27], s9 offen nt
	buffer_load_dword v4, v28, s[16:19], s7 offen nt
	buffer_load_dword v5, v28, s[16:19], s8 offen nt
	s_add_i32 s5, s34, -1
	s_max_i32 s5, s5, 0
	s_mul_i32 s6, s5, 0x804
	s_add_i32 s6, s6, s35
	s_add_i32 s7, s6, 0x505014
	s_add_i32 s8, s6, 0x606018
	s_mul_i32 s9, s5, 0x180c
	s_add_i32 s9, s9, s33
	s_add_i32 s4, s34, 0
	s_min_i32 s4, s4, 0x200
	s_mul_i32 s4, s4, 0x804
	s_add_i32 s4, s4, s38
	buffer_load_dword v16, v28, s[20:23], s4 offen nt
	buffer_load_dwordx3 v[12:14], v27, s[24:27], s9 offen nt
	buffer_load_dword v6, v28, s[16:19], s7 offen nt
	buffer_load_dword v7, v28, s[16:19], s8 offen nt
	s_waitcnt vmcnt(8)
	s_add_i32 s4, s34, -3
	s_cmpk_lt_u32 s4, 0x201
	s_cselect_b64 s[12:13], s[40:41], 0
	v_cmp_eq_u32_e64 s[14:15], s37, v29
	s_and_b64 s[14:15], s[14:15], s[12:13]
	v_cndmask_b32_e64 v17, 0, 1, s[14:15]
	s_add_i32 s4, s34, -2
	s_cmpk_lt_u32 s4, 0x201
	s_cselect_b64 s[12:13], s[40:41], 0
	v_cmp_eq_u32_e64 s[14:15], s37, v2
	s_and_b64 s[14:15], s[14:15], s[12:13]
	v_cndmask_b32_e64 v20, 0, 1, s[14:15]
	s_nop 0
	v_or_b32_dpp v21, v17, v17 wave_shr:1 row_mask:0xf bank_mask:0xf bound_ctrl:1
	v_or_b32_dpp v24, v20, v20 wave_shr:1 row_mask:0xf bank_mask:0xf bound_ctrl:1
	s_nop 1
	v_or_b32_dpp v21, v17, v21 wave_shl:1 row_mask:0xf bank_mask:0xf bound_ctrl:1
	v_or_b32_dpp v24, v20, v24 wave_shl:1 row_mask:0xf bank_mask:0xf bound_ctrl:1
	s_nop 1
	v_or_b32_dpp v25, v21, v21 wave_shr:1 row_mask:0xf bank_mask:0xf bound_ctrl:1
	v_or_b32_dpp v30, v24, v24 wave_shr:1 row_mask:0xf bank_mask:0xf bound_ctrl:1
	s_nop 1
	v_or_b32_dpp v25, v21, v25 wave_shl:1 row_mask:0xf bank_mask:0xf bound_ctrl:1
	v_or_b32_dpp v30, v24, v30 wave_shl:1 row_mask:0xf bank_mask:0xf bound_ctrl:1
	v_mov_b32_e32 v17, 0
	v_mov_b32_e32 v24, 0
	s_add_i32 s5, s34, 0
	s_min_i32 s5, s5, 0x200
	s_mul_i32 s6, s5, 0x804
	s_add_i32 s6, s6, s35
	s_add_i32 s7, s6, 0x505014
	s_add_i32 s8, s6, 0x606018
	s_mul_i32 s9, s5, 0x180c
	s_add_i32 s9, s9, s33
	s_add_i32 s4, s34, 1
	s_min_i32 s4, s4, 0x200
	s_mul_i32 s4, s4, 0x804
	s_add_i32 s4, s4, s38
	buffer_load_dword v31, v28, s[20:23], s4 offen nt
	buffer_load_dwordx3 v[32:34], v27, s[24:27], s9 offen nt
	buffer_load_dword v20, v28, s[16:19], s7 offen nt
	buffer_load_dword v21, v28, s[16:19], s8 offen nt
	s_waitcnt vmcnt(8)
	v_mov_b32_dpp v36, v8 wave_shr:1 row_mask:0xf bank_mask:0xf bound_ctrl:1
	v_mov_b32_dpp v37, v9 wave_shr:1 row_mask:0xf bank_mask:0xf bound_ctrl:1
	v_mov_b32_dpp v38, v10 wave_shr:1 row_mask:0xf bank_mask:0xf bound_ctrl:1
	v_mov_b32_dpp v40, v8 wave_shl:1 row_mask:0xf bank_mask:0xf bound_ctrl:1
	v_mov_b32_dpp v41, v9 wave_shl:1 row_mask:0xf bank_mask:0xf bound_ctrl:1
	v_mov_b32_dpp v42, v10 wave_shl:1 row_mask:0xf bank_mask:0xf bound_ctrl:1
	s_add_i32 s4, s34, -1
	s_cmpk_lt_u32 s4, 0x201
	s_cselect_b64 s[12:13], s[40:41], 0
	v_cmp_eq_u32_e64 s[14:15], s37, v3
	s_and_b64 s[14:15], s[14:15], s[12:13]
	v_cndmask_b32_e64 v44, 0, 1, s[14:15]
	v_pk_add_f32 v[46:47], v[8:9], v[36:37]
	v_pk_mul_f32 v[48:49], v[8:9], v[8:9] op_sel_hi:[0,1]
	v_or_b32_dpp v45, v44, v44 wave_shr:1 row_mask:0xf bank_mask:0xf bound_ctrl:1
	v_pk_mul_f32 v[50:51], v[8:9], v[10:11] op_sel_hi:[1,0]
	v_or_b32_dpp v45, v44, v45 wave_shl:1 row_mask:0xf bank_mask:0xf bound_ctrl:1
	v_mul_f32_e64 v52, v9, v9
	v_mul_f32_e64 v53, v10, v10
	v_or_b32_dpp v56, v45, v45 wave_shr:1 row_mask:0xf bank_mask:0xf bound_ctrl:1
	v_add_f32_e64 v54, v10, v38
	v_pk_add_f32 v[46:47], v[46:47], v[40:41]
	v_or_b32_dpp v56, v45, v56 wave_shl:1 row_mask:0xf bank_mask:0xf bound_ctrl:1
	v_or3_b32 v57, v56, v30, v25
	v_or3_b32 v57, v57, v17, v24
	s_add_i32 s4, s34, -4
	s_cmpk_lt_u32 s4, 0x1ff
	s_cselect_b64 s[12:13], s[42:43], 0
	v_cmp_ne_u32_e64 s[30:31], 0, v57
	s_and_b64 s[30:31], s[30:31], s[12:13]
	v_cndmask_b32_e64 v57, 0, 1.0, s[30:31]
	v_pk_fma_f32 v[48:49], v[36:37], v[36:37], v[48:49] op_sel_hi:[0,1,1]
	v_pk_fma_f32 v[50:51], v[36:37], v[38:39], v[50:51] op_sel_hi:[1,0,1]
	v_fma_f32 v52, v37, v37, v52
	v_fma_f32 v53, v38, v38, v53
	v_add_f32_dpp v55, v57, v57 wave_shr:1 row_mask:0xf bank_mask:0xf bound_ctrl:1
	v_add_f32_e64 v54, v54, v42
	v_pk_fma_f32 v[48:49], v[40:41], v[40:41], v[48:49] op_sel_hi:[0,1,1]
	v_pk_fma_f32 v[50:51], v[40:41], v[42:43], v[50:51] op_sel_hi:[1,0,1]
	v_fma_f32 v52, v41, v41, v52
	v_fma_f32 v53, v42, v42, v53
	v_add_f32_dpp v55, v57, v55 wave_shl:1 row_mask:0xf bank_mask:0xf bound_ctrl:1
	v_mov_b32_dpp v58, v4 wave_shr:1 row_mask:0xf bank_mask:0xf bound_ctrl:1
	v_mov_b32_dpp v59, v5 wave_shr:1 row_mask:0xf bank_mask:0xf bound_ctrl:1
	v_mov_b32_dpp v62, v4 wave_shl:1 row_mask:0xf bank_mask:0xf bound_ctrl:1
	v_mov_b32_dpp v63, v5 wave_shl:1 row_mask:0xf bank_mask:0xf bound_ctrl:1
	v_pk_mul_f32 v[44:45], v[4:5], v[8:9] op_sel_hi:[1,0]
	v_pk_mul_f32 v[60:61], v[4:5], v[8:9] op_sel:[0,1]
	v_pk_mul_f32 v[64:65], v[4:5], v[10:11] op_sel_hi:[1,0]
	v_pk_add_f32 v[68:69], v[4:5], v[58:59]
	v_pk_fma_f32 v[44:45], v[58:59], v[36:37], v[44:45] op_sel_hi:[1,0,1]
	v_pk_fma_f32 v[60:61], v[58:59], v[36:37], v[60:61] op_sel:[0,1,0]
	v_pk_fma_f32 v[64:65], v[58:59], v[38:39], v[64:65] op_sel_hi:[1,0,1]
	v_pk_add_f32 v[68:69], v[68:69], v[62:63]
	v_pk_fma_f32 v[44:45], v[62:63], v[40:41], v[44:45] op_sel_hi:[1,0,1]
	v_pk_fma_f32 v[60:61], v[62:63], v[40:41], v[60:61] op_sel:[0,1,0]
	v_pk_fma_f32 v[64:65], v[62:63], v[42:43], v[64:65] op_sel_hi:[1,0,1]
	s_barrier
	s_add_i32 s5, s34, 1
	s_min_i32 s5, s5, 0x200
	s_mul_i32 s6, s5, 0x804
	s_add_i32 s6, s6, s35
	s_add_i32 s7, s6, 0x505014
	s_add_i32 s8, s6, 0x606018
	s_mul_i32 s9, s5, 0x180c
	s_add_i32 s9, s9, s33
	s_add_i32 s4, s34, 2
	s_min_i32 s4, s4, 0x200
	s_mul_i32 s4, s4, 0x804
	s_add_i32 s4, s4, s38
	buffer_load_dword v24, v28, s[20:23], s4 offen nt
	buffer_load_dwordx3 v[72:74], v27, s[24:27], s9 offen nt
	buffer_load_dword v58, v28, s[16:19], s7 offen nt
	buffer_load_dword v59, v28, s[16:19], s8 offen nt
	s_waitcnt vmcnt(8)
	v_mov_b32_dpp v76, v12 wave_shr:1 row_mask:0xf bank_mask:0xf bound_ctrl:1
	v_mov_b32_dpp v77, v13 wave_shr:1 row_mask:0xf bank_mask:0xf bound_ctrl:1
	v_mov_b32_dpp v78, v14 wave_shr:1 row_mask:0xf bank_mask:0xf bound_ctrl:1
	v_mov_b32_dpp v80, v12 wave_shl:1 row_mask:0xf bank_mask:0xf bound_ctrl:1
	v_mov_b32_dpp v81, v13 wave_shl:1 row_mask:0xf bank_mask:0xf bound_ctrl:1
	v_mov_b32_dpp v82, v14 wave_shl:1 row_mask:0xf bank_mask:0xf bound_ctrl:1
	s_add_i32 s4, s34, 0
	s_cmpk_lt_u32 s4, 0x201
	s_cselect_b64 s[12:13], s[40:41], 0
	v_cmp_eq_u32_e64 s[14:15], s37, v16
	s_and_b64 s[14:15], s[14:15], s[12:13]
	v_cndmask_b32_e64 v57, 0, 1, s[14:15]
	v_pk_add_f32 v[62:63], v[12:13], v[76:77]
	v_pk_mul_f32 v[66:67], v[12:13], v[12:13] op_sel_hi:[0,1]
	v_or_b32_dpp v88, v57, v57 wave_shr:1 row_mask:0xf bank_mask:0xf bound_ctrl:1
	v_pk_mul_f32 v[70:71], v[12:13], v[14:15] op_sel_hi:[1,0]
	v_or_b32_dpp v88, v57, v88 wave_shl:1 row_mask:0xf bank_mask:0xf bound_ctrl:1
	v_mul_f32_e64 v84, v13, v13
	v_mul_f32_e64 v85, v14, v14
	v_or_b32_dpp v89, v88, v88 wave_shr:1 row_mask:0xf bank_mask:0xf bound_ctrl:1
	v_add_f32_e64 v86, v14, v78
	v_pk_add_f32 v[62:63], v[62:63], v[80:81]
	v_or_b32_dpp v89, v88, v89 wave_shl:1 row_mask:0xf bank_mask:0xf bound_ctrl:1
	v_or3_b32 v57, v89, v56, v30
	v_or3_b32 v57, v57, v25, v17
	s_add_i32 s4, s34, -3
	s_cmpk_lt_u32 s4, 0x1ff
	s_cselect_b64 s[12:13], s[42:43], 0
	v_cmp_ne_u32_e64 s[30:31], 0, v57
	s_and_b64 s[30:31], s[30:31], s[12:13]
	v_cndmask_b32_e64 v57, 0, 1.0, s[30:31]
	v_pk_fma_f32 v[66:67], v[76:77], v[76:77], v[66:67] op_sel_hi:[0,1,1]
	v_pk_fma_f32 v[70:71], v[76:77], v[78:79], v[70:71] op_sel_hi:[1,0,1]
	v_fma_f32 v84, v77, v77, v84
	v_fma_f32 v85, v78, v78, v85
	v_add_f32_dpp v87, v57, v57 wave_shr:1 row_mask:0xf bank_mask:0xf bound_ctrl:1
	v_add_f32_e64 v86, v86, v82
	v_pk_fma_f32 v[66:67], v[80:81], v[80:81], v[66:67] op_sel_hi:[0,1,1]
	v_pk_fma_f32 v[70:71], v[80:81], v[82:83], v[70:71] op_sel_hi:[1,0,1]
	v_fma_f32 v84, v81, v81, v84
	v_fma_f32 v85, v82, v82, v85
	v_add_f32_dpp v87, v57, v87 wave_shl:1 row_mask:0xf bank_mask:0xf bound_ctrl:1
	v_mov_b32_dpp v92, v6 wave_shr:1 row_mask:0xf bank_mask:0xf bound_ctrl:1
	v_mov_b32_dpp v93, v7 wave_shr:1 row_mask:0xf bank_mask:0xf bound_ctrl:1
	v_mov_b32_dpp v96, v6 wave_shl:1 row_mask:0xf bank_mask:0xf bound_ctrl:1
	v_mov_b32_dpp v97, v7 wave_shl:1 row_mask:0xf bank_mask:0xf bound_ctrl:1
	v_pk_mul_f32 v[90:91], v[6:7], v[12:13] op_sel_hi:[1,0]
	v_pk_mul_f32 v[94:95], v[6:7], v[12:13] op_sel:[0,1]
	v_pk_mul_f32 v[98:99], v[6:7], v[14:15] op_sel_hi:[1,0]
	v_pk_add_f32 v[102:103], v[6:7], v[92:93]
	v_pk_fma_f32 v[90:91], v[92:93], v[76:77], v[90:91] op_sel_hi:[1,0,1]
	v_pk_fma_f32 v[94:95], v[92:93], v[76:77], v[94:95] op_sel:[0,1,0]
	v_pk_fma_f32 v[98:99], v[92:93], v[78:79], v[98:99] op_sel_hi:[1,0,1]
	v_pk_add_f32 v[102:103], v[102:103], v[96:97]
	v_pk_fma_f32 v[90:91], v[96:97], v[80:81], v[90:91] op_sel_hi:[1,0,1]
	v_pk_fma_f32 v[94:95], v[96:97], v[80:81], v[94:95] op_sel:[0,1,0]
	v_pk_fma_f32 v[98:99], v[96:97], v[82:83], v[98:99] op_sel_hi:[1,0,1]
	s_barrier
	s_add_i32 s5, s34, 2
	s_min_i32 s5, s5, 0x200
	s_mul_i32 s6, s5, 0x804
	s_add_i32 s6, s6, s35
	s_add_i32 s7, s6, 0x505014
	s_add_i32 s8, s6, 0x606018
	s_mul_i32 s9, s5, 0x180c
	s_add_i32 s9, s9, s33
	s_add_i32 s4, s34, 3
	s_min_i32 s4, s4, 0x200
	s_mul_i32 s4, s4, 0x804
	s_add_i32 s4, s4, s38
	buffer_load_dword v17, v28, s[20:23], s4 offen nt
	buffer_load_dwordx3 v[104:106], v27, s[24:27], s9 offen nt
	buffer_load_dword v92, v28, s[16:19], s7 offen nt
	buffer_load_dword v93, v28, s[16:19], s8 offen nt
	s_waitcnt vmcnt(8)
	v_mov_b32_dpp v108, v32 wave_shr:1 row_mask:0xf bank_mask:0xf bound_ctrl:1
	v_mov_b32_dpp v109, v33 wave_shr:1 row_mask:0xf bank_mask:0xf bound_ctrl:1
	v_mov_b32_dpp v110, v34 wave_shr:1 row_mask:0xf bank_mask:0xf bound_ctrl:1
	v_mov_b32_dpp v112, v32 wave_shl:1 row_mask:0xf bank_mask:0xf bound_ctrl:1
	v_mov_b32_dpp v113, v33 wave_shl:1 row_mask:0xf bank_mask:0xf bound_ctrl:1
	v_mov_b32_dpp v114, v34 wave_shl:1 row_mask:0xf bank_mask:0xf bound_ctrl:1
	s_add_i32 s4, s34, 1
	s_cmpk_lt_u32 s4, 0x201
	s_cselect_b64 s[12:13], s[40:41], 0
	v_cmp_eq_u32_e64 s[14:15], s37, v31
	s_and_b64 s[14:15], s[14:15], s[12:13]
	v_cndmask_b32_e64 v29, 0, 1, s[14:15]
	v_pk_add_f32 v[96:97], v[32:33], v[108:109]
	v_pk_mul_f32 v[100:101], v[32:33], v[32:33] op_sel_hi:[0,1]
	v_or_b32_dpp v57, v29, v29 wave_shr:1 row_mask:0xf bank_mask:0xf bound_ctrl:1
	v_pk_mul_f32 v[116:117], v[32:33], v[34:35] op_sel_hi:[1,0]
	v_or_b32_dpp v57, v29, v57 wave_shl:1 row_mask:0xf bank_mask:0xf bound_ctrl:1
	v_mul_f32_e64 v118, v33, v33
	v_mul_f32_e64 v119, v34, v34
	v_or_b32_dpp v88, v57, v57 wave_shr:1 row_mask:0xf bank_mask:0xf bound_ctrl:1
	v_add_f32_e64 v120, v34, v110
	v_pk_add_f32 v[96:97], v[96:97], v[112:113]
	v_or_b32_dpp v88, v57, v88 wave_shl:1 row_mask:0xf bank_mask:0xf bound_ctrl:1
	v_or3_b32 v29, v88, v89, v56
	v_or3_b32 v29, v29, v30, v25
	s_add_i32 s4, s34, -2
	s_cmpk_lt_u32 s4, 0x1ff
	s_cselect_b64 s[12:13], s[42:43], 0
	v_cmp_ne_u32_e64 s[30:31], 0, v29
	s_and_b64 s[30:31], s[30:31], s[12:13]
	v_cndmask_b32_e64 v29, 0, 1.0, s[30:31]
	v_pk_fma_f32 v[100:101], v[108:109], v[108:109], v[100:101] op_sel_hi:[0,1,1]
	v_pk_fma_f32 v[116:117], v[108:109], v[110:111], v[116:117] op_sel_hi:[1,0,1]
	v_fma_f32 v118, v109, v109, v118
	v_fma_f32 v119, v110, v110, v119
	v_add_f32_dpp v121, v29, v29 wave_shr:1 row_mask:0xf bank_mask:0xf bound_ctrl:1
	v_add_f32_e64 v120, v120, v114
	v_pk_fma_f32 v[100:101], v[112:113], v[112:113], v[100:101] op_sel_hi:[0,1,1]
	v_pk_fma_f32 v[116:117], v[112:113], v[114:115], v[116:117] op_sel_hi:[1,0,1]
	v_fma_f32 v118, v113, v113, v118
	v_fma_f32 v119, v114, v114, v119
	v_add_f32_dpp v121, v29, v121 wave_shl:1 row_mask:0xf bank_mask:0xf bound_ctrl:1
	v_pk_add_f32 v[124:125], v[62:63], v[96:97]
	v_pk_add_f32 v[122:123], v[46:47], v[124:125]
	v_pk_add_f32 v[46:47], v[66:67], v[100:101]
	v_pk_add_f32 v[62:63], v[48:49], v[46:47]
	v_pk_add_f32 v[48:49], v[70:71], v[116:117]
	v_pk_add_f32 v[66:67], v[50:51], v[48:49]
	v_pk_add_f32 v[50:51], v[84:85], v[118:119]
	v_pk_add_f32 v[70:71], v[52:53], v[50:51]
	v_pk_add_f32 v[52:53], v[86:87], v[120:121]
	v_pk_add_f32 v[84:85], v[54:55], v[52:53]
	v_mul_f32_e64 v128, v122, v22
	v_mul_f32_e64 v129, v123, v22
	v_mul_f32_e64 v130, v84, v22
	v_fma_f32 v29, v62, v22, v26
	v_mul_f32_e64 v57, v63, v22
	v_mul_f32_e64 v54, v66, v22
	v_fma_f32 v55, v70, v22, v26
	v_mul_f32_e64 v86, v67, v22
	v_fma_f32 v87, v71, v22, v26
	v_fma_f32 v29, -v128, v128, v29
	v_fma_f32 v57, -v128, v129, v57
	v_fma_f32 v54, -v128, v130, v54
	v_fma_f32 v55, -v129, v129, v55
	v_fma_f32 v86, -v129, v130, v86
	v_fma_f32 v87, -v130, v130, v87
	v_mul_f32_e64 v126, v86, v86
	v_mul_f32_e64 v127, v57, v87
	v_mul_f32_e64 v140, v54, v55
	v_mul_f32_e64 v141, v54, v54
	v_mul_f32_e64 v142, v29, v86
	v_mul_f32_e64 v143, v57, v57
	v_fma_f32 v126, v55, v87, -v126
	v_fma_f32 v127, v54, v86, -v127
	v_fma_f32 v140, v57, v86, -v140
	v_fma_f32 v141, v29, v87, -v141
	v_fma_f32 v142, v57, v54, -v142
	v_fma_f32 v143, v29, v55, -v143
	v_mul_f32_e64 v144, v29, v126
	v_fma_f32 v144, v57, v127, v144
	v_fma_f32 v144, v54, v140, v144
	v_rcp_f32_e32 v144, v144
	v_cmp_ne_u32_e64 vcc, s37, v2
	v_mul_f32_e64 v144, v144, v22
	v_cndmask_b32_e64 v144, 0, v144, s[30:31]
	v_cndmask_b32_e64 v29, 0, v18, vcc
	v_cndmask_b32_e64 v137, 0, v22, s[30:31]
	v_mul_f32_e64 v131, v126, v144
	v_mul_f32_e64 v132, v127, v144
	v_mul_f32_e64 v133, v140, v144
	v_mul_f32_e64 v134, v141, v144
	v_mul_f32_e64 v135, v142, v144
	v_mul_f32_e64 v136, v143, v144
	v_add_f32_e64 v138, v85, v29
	v_mov_b32_e32 v139, v2
	ds_write_b128 v23, v[128:131]
	ds_write_b128 v23, v[132:135] offset:1024
	ds_write_b128 v23, v[136:139] offset:2048
	v_mov_b32_dpp v54, v20 wave_shr:1 row_mask:0xf bank_mask:0xf bound_ctrl:1
	v_mov_b32_dpp v55, v21 wave_shr:1 row_mask:0xf bank_mask:0xf bound_ctrl:1
	v_mov_b32_dpp v62, v20 wave_shl:1 row_mask:0xf bank_mask:0xf bound_ctrl:1
	v_mov_b32_dpp v63, v21 wave_shl:1 row_mask:0xf bank_mask:0xf bound_ctrl:1
	v_pk_mul_f32 v[84:85], v[20:21], v[32:33] op_sel_hi:[1,0]
	v_pk_mul_f32 v[140:141], v[20:21], v[32:33] op_sel:[0,1]
	v_pk_mul_f32 v[144:145], v[20:21], v[34:35] op_sel_hi:[1,0]
	v_pk_add_f32 v[148:149], v[20:21], v[54:55]
	v_pk_fma_f32 v[84:85], v[54:55], v[108:109], v[84:85] op_sel_hi:[1,0,1]
	v_pk_fma_f32 v[140:141], v[54:55], v[108:109], v[140:141] op_sel:[0,1,0]
	v_pk_fma_f32 v[144:145], v[54:55], v[110:111], v[144:145] op_sel_hi:[1,0,1]
	v_pk_add_f32 v[148:149], v[148:149], v[62:63]
	v_pk_fma_f32 v[84:85], v[62:63], v[112:113], v[84:85] op_sel_hi:[1,0,1]
	v_pk_fma_f32 v[140:141], v[62:63], v[112:113], v[140:141] op_sel:[0,1,0]
	v_pk_fma_f32 v[144:145], v[62:63], v[114:115], v[144:145] op_sel_hi:[1,0,1]
	s_waitcnt lgkmcnt(0)
	s_barrier
	v_pk_add_f32 v[54:55], v[102:103], v[148:149]
	v_pk_add_f32 v[62:63], v[68:69], v[54:55]
	v_pk_add_f32 v[66:67], v[90:91], v[84:85]
	v_pk_add_f32 v[68:69], v[44:45], v[66:67]
	v_pk_add_f32 v[70:71], v[94:95], v[140:141]
	v_pk_add_f32 v[44:45], v[60:61], v[70:71]
	v_pk_add_f32 v[86:87], v[98:99], v[144:145]
	v_pk_add_f32 v[60:61], v[64:65], v[86:87]
	v_pk_fma_f32 v[68:69], v[128:129], v[62:63], v[68:69] op_sel_hi:[0,1,1] neg_lo:[1,0,0] neg_hi:[1,0,0]
	v_pk_fma_f32 v[44:45], v[128:129], v[62:63], v[44:45] op_sel:[1,0,0] neg_lo:[1,0,0] neg_hi:[1,0,0]
	v_pk_fma_f32 v[60:61], v[130:131], v[62:63], v[60:61] op_sel_hi:[0,1,1] neg_lo:[1,0,0] neg_hi:[1,0,0]
	v_pk_mul_f32 v[90:91], v[130:131], v[68:69] op_sel:[1,0]
	v_pk_mul_f32 v[94:95], v[132:133], v[68:69] op_sel_hi:[0,1]
	v_pk_mul_f32 v[98:99], v[132:133], v[68:69] op_sel:[1,0]
	v_pk_fma_f32 v[90:91], v[132:133], v[44:45], v[90:91] op_sel_hi:[0,1,1]
	v_pk_fma_f32 v[94:95], v[134:135], v[44:45], v[94:95] op_sel_hi:[0,1,1]
	v_pk_fma_f32 v[98:99], v[134:135], v[44:45], v[98:99] op_sel:[1,0,0]
	v_pk_fma_f32 v[90:91], v[132:133], v[60:61], v[90:91] op_sel:[1,0,0]
	v_pk_fma_f32 v[94:95], v[134:135], v[60:61], v[94:95] op_sel:[1,0,0]
	v_pk_fma_f32 v[98:99], v[136:137], v[60:61], v[98:99] op_sel_hi:[0,1,1]
	v_pk_mul_f32 v[64:65], v[128:129], v[90:91] op_sel_hi:[0,1]
	v_pk_fma_f32 v[64:65], v[128:129], v[94:95], v[64:65] op_sel:[1,0,0]
	v_pk_fma_f32 v[64:65], v[130:131], v[98:99], v[64:65] op_sel_hi:[0,1,1]
	v_pk_fma_f32 v[64:65], v[136:137], v[62:63], v[64:65] op_sel:[1,0,0] neg_lo:[0,0,1] neg_hi:[0,0,1]
	s_add_i32 s5, s34, 3
	s_min_i32 s5, s5, 0x200
	s_mul_i32 s6, s5, 0x804
	s_add_i32 s6, s6, s35
	s_add_i32 s7, s6, 0x505014
	s_add_i32 s8, s6, 0x606018
	s_mul_i32 s9, s5, 0x180c
	s_add_i32 s9, s9, s33
	s_add_i32 s4, s34, 4
	s_min_i32 s4, s4, 0x200
	s_mul_i32 s4, s4, 0x804
	s_add_i32 s4, s4, s38
	buffer_load_dword v2, v28, s[20:23], s4 offen nt
	buffer_load_dwordx3 v[8:10], v27, s[24:27], s9 offen nt
	buffer_load_dword v4, v28, s[16:19], s7 offen nt
	buffer_load_dword v5, v28, s[16:19], s8 offen nt
	s_waitcnt vmcnt(8)
	v_mov_b32_dpp v36, v72 wave_shr:1 row_mask:0xf bank_mask:0xf bound_ctrl:1
	v_mov_b32_dpp v37, v73 wave_shr:1 row_mask:0xf bank_mask:0xf bound_ctrl:1
	v_mov_b32_dpp v38, v74 wave_shr:1 row_mask:0xf bank_mask:0xf bound_ctrl:1
	v_mov_b32_dpp v40, v72 wave_shl:1 row_mask:0xf bank_mask:0xf bound_ctrl:1
	v_mov_b32_dpp v41, v73 wave_shl:1 row_mask:0xf bank_mask:0xf bound_ctrl:1
	v_mov_b32_dpp v42, v74 wave_shl:1 row_mask:0xf bank_mask:0xf bound_ctrl:1
	s_add_i32 s4, s34, 2
	s_cmpk_lt_u32 s4, 0x201
	s_cselect_b64 s[12:13], s[40:41], 0
	v_cmp_eq_u32_e64 s[14:15], s37, v24
	s_and_b64 s[14:15], s[14:15], s[12:13]
	v_cndmask_b32_e64 v25, 0, 1, s[14:15]
	v_pk_add_f32 v[44:45], v[72:73], v[36:37]
	v_pk_mul_f32 v[60:61], v[72:73], v[72:73] op_sel_hi:[0,1]
	v_or_b32_dpp v29, v25, v25 wave_shr:1 row_mask:0xf bank_mask:0xf bound_ctrl:1
	v_pk_mul_f32 v[62:63], v[72:73], v[74:75] op_sel_hi:[1,0]
	v_or_b32_dpp v29, v25, v29 wave_shl:1 row_mask:0xf bank_mask:0xf bound_ctrl:1
	v_mul_f32_e64 v68, v73, v73
	v_mul_f32_e64 v69, v74, v74
	v_or_b32_dpp v57, v29, v29 wave_shr:1 row_mask:0xf bank_mask:0xf bound_ctrl:1
	v_add_f32_e64 v102, v74, v38
	v_pk_add_f32 v[44:45], v[44:45], v[40:41]
	v_or_b32_dpp v57, v29, v57 wave_shl:1 row_mask:0xf bank_mask:0xf bound_ctrl:1
	v_or3_b32 v25, v57, v88, v89
	v_or3_b32 v25, v25, v56, v30
	s_add_i32 s4, s34, -1
	s_cmpk_lt_u32 s4, 0x1ff
	s_cselect_b64 s[12:13], s[42:43], 0
	v_cmp_ne_u32_e64 s[30:31], 0, v25
	s_and_b64 s[30:31], s[30:31], s[12:13]
	v_cndmask_b32_e64 v25, 0, 1.0, s[30:31]
	v_pk_fma_f32 v[60:61], v[36:37], v[36:37], v[60:61] op_sel_hi:[0,1,1]
	v_pk_fma_f32 v[62:63], v[36:37], v[38:39], v[62:63] op_sel_hi:[1,0,1]
	v_fma_f32 v68, v37, v37, v68
	v_fma_f32 v69, v38, v38, v69
	v_add_f32_dpp v103, v25, v25 wave_shr:1 row_mask:0xf bank_mask:0xf bound_ctrl:1
	v_add_f32_e64 v102, v102, v42
	v_pk_fma_f32 v[60:61], v[40:41], v[40:41], v[60:61] op_sel_hi:[0,1,1]
	v_pk_fma_f32 v[62:63], v[40:41], v[42:43], v[62:63] op_sel_hi:[1,0,1]
	v_fma_f32 v68, v41, v41, v68
	v_fma_f32 v69, v42, v42, v69
	v_add_f32_dpp v103, v25, v103 wave_shl:1 row_mask:0xf bank_mask:0xf bound_ctrl:1
	v_pk_add_f32 v[122:123], v[124:125], v[44:45]
	v_pk_add_f32 v[124:125], v[46:47], v[60:61]
	v_pk_add_f32 v[46:47], v[48:49], v[62:63]
	v_pk_add_f32 v[48:49], v[50:51], v[68:69]
	v_pk_add_f32 v[50:51], v[52:53], v[102:103]
	v_mul_f32_e64 v128, v122, v22
	v_mul_f32_e64 v129, v123, v22
	v_mul_f32_e64 v130, v50, v22
	v_fma_f32 v25, v124, v22, v26
	v_mul_f32_e64 v29, v125, v22
	v_mul_f32_e64 v52, v46, v22
	v_fma_f32 v53, v48, v22, v26
	v_mul_f32_e64 v126, v47, v22
	v_fma_f32 v127, v49, v22, v26
	v_fma_f32 v25, -v128, v128, v25
	v_fma_f32 v29, -v128, v129, v29
	v_fma_f32 v52, -v128, v130, v52
	v_fma_f32 v53, -v129, v129, v53
	v_fma_f32 v126, -v129, v130, v126
	v_fma_f32 v127, -v130, v130, v127
	v_mul_f32_e64 v142, v126, v126
	v_mul_f32_e64 v143, v29, v127
	v_mul_f32_e64 v146, v52, v53
	v_mul_f32_e64 v147, v52, v52
	v_mul_f32_e64 v150, v25, v126
	v_mul_f32_e64 v151, v29, v29
	v_fma_f32 v142, v53, v127, -v142
	v_fma_f32 v143, v52, v126, -v143
	v_fma_f32 v146, v29, v126, -v146
	v_fma_f32 v147, v25, v127, -v147
	v_fma_f32 v150, v29, v52, -v150
	v_fma_f32 v151, v25, v53, -v151
	v_mul_f32_e64 v152, v25, v142
	v_fma_f32 v152, v29, v143, v152
	v_fma_f32 v152, v52, v146, v152
	v_rcp_f32_e32 v152, v152
	v_cmp_ne_u32_e64 vcc, s37, v3
	v_mul_f32_e64 v152, v152, v22
	v_cndmask_b32_e64 v152, 0, v152, s[30:31]
	v_cndmask_b32_e64 v25, 0, v18, vcc
	v_cndmask_b32_e64 v137, 0, v22, s[30:31]
	v_mul_f32_e64 v131, v142, v152
	v_mul_f32_e64 v132, v143, v152
	v_mul_f32_e64 v133, v146, v152
	v_mul_f32_e64 v134, v147, v152
	v_mul_f32_e64 v135, v150, v152
	v_mul_f32_e64 v136, v151, v152
	v_add_f32_e64 v138, v51, v25
	v_mov_b32_e32 v139, v3
	ds_write_b128 v23, v[128:131] offset:3072
	ds_write_b128 v23, v[132:135] offset:4096
	ds_write_b128 v23, v[136:139] offset:5120
	v_mov_b32_dpp v48, v58 wave_shr:1 row_mask:0xf bank_mask:0xf bound_ctrl:1
	v_mov_b32_dpp v49, v59 wave_shr:1 row_mask:0xf bank_mask:0xf bound_ctrl:1
	v_mov_b32_dpp v52, v58 wave_shl:1 row_mask:0xf bank_mask:0xf bound_ctrl:1
	v_mov_b32_dpp v53, v59 wave_shl:1 row_mask:0xf bank_mask:0xf bound_ctrl:1
	v_pk_mul_f32 v[46:47], v[58:59], v[72:73] op_sel_hi:[1,0]
	v_pk_mul_f32 v[50:51], v[58:59], v[72:73] op_sel:[0,1]
	v_pk_mul_f32 v[122:123], v[58:59], v[74:75] op_sel_hi:[1,0]
	v_pk_add_f32 v[126:127], v[58:59], v[48:49]
	v_pk_fma_f32 v[46:47], v[48:49], v[36:37], v[46:47] op_sel_hi:[1,0,1]
	v_pk_fma_f32 v[50:51], v[48:49], v[36:37], v[50:51] op_sel:[0,1,0]
	v_pk_fma_f32 v[122:123], v[48:49], v[38:39], v[122:123] op_sel_hi:[1,0,1]
	v_pk_add_f32 v[126:127], v[126:127], v[52:53]
	v_pk_fma_f32 v[46:47], v[52:53], v[40:41], v[46:47] op_sel_hi:[1,0,1]
	v_pk_fma_f32 v[50:51], v[52:53], v[40:41], v[50:51] op_sel:[0,1,0]
	v_pk_fma_f32 v[122:123], v[52:53], v[42:43], v[122:123] op_sel_hi:[1,0,1]
	s_waitcnt lgkmcnt(0)
	s_barrier
	v_pk_add_f32 v[48:49], v[54:55], v[126:127]
	v_pk_add_f32 v[54:55], v[66:67], v[46:47]
	v_pk_add_f32 v[66:67], v[70:71], v[50:51]
	v_pk_add_f32 v[70:71], v[86:87], v[122:123]
	v_pk_fma_f32 v[54:55], v[128:129], v[48:49], v[54:55] op_sel_hi:[0,1,1] neg_lo:[1,0,0] neg_hi:[1,0,0]
	v_pk_fma_f32 v[66:67], v[128:129], v[48:49], v[66:67] op_sel:[1,0,0] neg_lo:[1,0,0] neg_hi:[1,0,0]
	v_pk_fma_f32 v[70:71], v[130:131], v[48:49], v[70:71] op_sel_hi:[0,1,1] neg_lo:[1,0,0] neg_hi:[1,0,0]
	v_pk_mul_f32 v[52:53], v[130:131], v[54:55] op_sel:[1,0]
	v_pk_mul_f32 v[124:125], v[132:133], v[54:55] op_sel_hi:[0,1]
	v_pk_mul_f32 v[152:153], v[132:133], v[54:55] op_sel:[1,0]
	v_pk_fma_f32 v[52:53], v[132:133], v[66:67], v[52:53] op_sel_hi:[0,1,1]
	v_pk_fma_f32 v[124:125], v[134:135], v[66:67], v[124:125] op_sel_hi:[0,1,1]
	v_pk_fma_f32 v[152:153], v[134:135], v[66:67], v[152:153] op_sel:[1,0,0]
	v_pk_fma_f32 v[52:53], v[132:133], v[70:71], v[52:53] op_sel:[1,0,0]
	v_pk_fma_f32 v[124:125], v[134:135], v[70:71], v[124:125] op_sel:[1,0,0]
	v_pk_fma_f32 v[152:153], v[136:137], v[70:71], v[152:153] op_sel_hi:[0,1,1]
	v_pk_mul_f32 v[86:87], v[128:129], v[52:53] op_sel_hi:[0,1]
	v_pk_fma_f32 v[86:87], v[128:129], v[124:125], v[86:87] op_sel:[1,0,0]
	v_pk_fma_f32 v[86:87], v[130:131], v[152:153], v[86:87] op_sel_hi:[0,1,1]
	v_pk_fma_f32 v[86:87], v[136:137], v[48:49], v[86:87] op_sel:[1,0,0] neg_lo:[0,0,1] neg_hi:[0,0,1]
	s_add_i32 s5, s34, 4
	s_min_i32 s5, s5, 0x200
	s_mul_i32 s6, s5, 0x804
	s_add_i32 s6, s6, s35
	s_add_i32 s7, s6, 0x505014
	s_add_i32 s8, s6, 0x606018
	s_mul_i32 s9, s5, 0x180c
	s_add_i32 s9, s9, s33
	s_add_i32 s4, s34, 5
	s_min_i32 s4, s4, 0x200
	s_mul_i32 s4, s4, 0x804
	s_add_i32 s4, s4, s38
	buffer_load_dword v3, v28, s[20:23], s4 offen nt
	buffer_load_dwordx3 v[12:14], v27, s[24:27], s9 offen nt
	buffer_load_dword v6, v28, s[16:19], s7 offen nt
	buffer_load_dword v7, v28, s[16:19], s8 offen nt
	s_waitcnt vmcnt(8)
	v_mov_b32_dpp v76, v104 wave_shr:1 row_mask:0xf bank_mask:0xf bound_ctrl:1
	v_mov_b32_dpp v77, v105 wave_shr:1 row_mask:0xf bank_mask:0xf bound_ctrl:1
	v_mov_b32_dpp v78, v106 wave_shr:1 row_mask:0xf bank_mask:0xf bound_ctrl:1
	v_mov_b32_dpp v80, v104 wave_shl:1 row_mask:0xf bank_mask:0xf bound_ctrl:1
	v_mov_b32_dpp v81, v105 wave_shl:1 row_mask:0xf bank_mask:0xf bound_ctrl:1
	v_mov_b32_dpp v82, v106 wave_shl:1 row_mask:0xf bank_mask:0xf bound_ctrl:1
	s_add_i32 s4, s34, 3
	s_cmpk_lt_u32 s4, 0x201
	s_cselect_b64 s[12:13], s[40:41], 0
	v_cmp_eq_u32_e64 s[14:15], s37, v17
	s_and_b64 s[14:15], s[14:15], s[12:13]
	v_cndmask_b32_e64 v25, 0, 1, s[14:15]
	v_pk_add_f32 v[48:49], v[104:105], v[76:77]
	v_pk_mul_f32 v[54:55], v[104:105], v[104:105] op_sel_hi:[0,1]
	v_or_b32_dpp v29, v25, v25 wave_shr:1 row_mask:0xf bank_mask:0xf bound_ctrl:1
	v_pk_mul_f32 v[66:67], v[104:105], v[106:107] op_sel_hi:[1,0]
	v_or_b32_dpp v29, v25, v29 wave_shl:1 row_mask:0xf bank_mask:0xf bound_ctrl:1
	v_mul_f32_e64 v70, v105, v105
	v_mul_f32_e64 v71, v106, v106
	v_or_b32_dpp v30, v29, v29 wave_shr:1 row_mask:0xf bank_mask:0xf bound_ctrl:1
	v_add_f32_e64 v128, v106, v78
	v_pk_add_f32 v[48:49], v[48:49], v[80:81]
	v_or_b32_dpp v30, v29, v30 wave_shl:1 row_mask:0xf bank_mask:0xf bound_ctrl:1
	v_or3_b32 v25, v30, v57, v88
	v_or3_b32 v25, v25, v89, v56
	s_add_i32 s4, s34, 0
	s_cmpk_lt_u32 s4, 0x1ff
	s_cselect_b64 s[12:13], s[42:43], 0
	v_cmp_ne_u32_e64 s[30:31], 0, v25
	s_and_b64 s[30:31], s[30:31], s[12:13]
	v_cndmask_b32_e64 v25, 0, 1.0, s[30:31]
	v_pk_fma_f32 v[54:55], v[76:77], v[76:77], v[54:55] op_sel_hi:[0,1,1]
	v_pk_fma_f32 v[66:67], v[76:77], v[78:79], v[66:67] op_sel_hi:[1,0,1]
	v_fma_f32 v70, v77, v77, v70
	v_fma_f32 v71, v78, v78, v71
	v_add_f32_dpp v129, v25, v25 wave_shr:1 row_mask:0xf bank_mask:0xf bound_ctrl:1
	v_add_f32_e64 v128, v128, v82
	v_pk_fma_f32 v[54:55], v[80:81], v[80:81], v[54:55] op_sel_hi:[0,1,1]
	v_pk_fma_f32 v[66:67], v[80:81], v[82:83], v[66:67] op_sel_hi:[1,0,1]
	v_fma_f32 v70, v81, v81, v70
	v_fma_f32 v71, v82, v82, v71
	v_add_f32_dpp v129, v25, v129 wave_shl:1 row_mask:0xf bank_mask:0xf bound_ctrl:1
	v_pk_add_f32 v[130:131], v[44:45], v[48:49]
	v_pk_add_f32 v[132:133], v[96:97], v[130:131]
	v_pk_add_f32 v[134:135], v[60:61], v[54:55]
	v_pk_add_f32 v[44:45], v[100:101], v[134:135]
	v_pk_add_f32 v[138:139], v[62:63], v[66:67]
	v_pk_add_f32 v[60:61], v[116:117], v[138:139]
	v_pk_add_f32 v[96:97], v[68:69], v[70:71]
	v_pk_add_f32 v[62:63], v[118:119], v[96:97]
	v_pk_add_f32 v[118:119], v[102:103], v[128:129]
	v_pk_add_f32 v[68:69], v[120:121], v[118:119]
	v_mul_f32_e64 v100, v132, v22
	v_mul_f32_e64 v101, v133, v22
	v_mul_f32_e64 v102, v68, v22
	v_fma_f32 v25, v44, v22, v26
	v_mul_f32_e64 v29, v45, v22
	v_mul_f32_e64 v116, v60, v22
	v_fma_f32 v117, v62, v22, v26
	v_mul_f32_e64 v120, v61, v22
	v_fma_f32 v121, v63, v22, v26
	v_fma_f32 v25, -v100, v100, v25
	v_fma_f32 v29, -v100, v101, v29
	v_fma_f32 v116, -v100, v102, v116
	v_fma_f32 v117, -v101, v101, v117
	v_fma_f32 v120, -v101, v102, v120
	v_fma_f32 v121, -v102, v102, v121
	v_mul_f32_e64 v136, v120, v120
	v_mul_f32_e64 v137, v29, v121
	v_mul_f32_e64 v142, v116, v117
	v_mul_f32_e64 v143, v116, v116
	v_mul_f32_e64 v146, v25, v120
	v_mul_f32_e64 v147, v29, v29
	v_fma_f32 v136, v117, v121, -v136
	v_fma_f32 v137, v116, v120, -v137
	v_fma_f32 v142, v29, v120, -v142
	v_fma_f32 v143, v25, v121, -v143
	v_fma_f32 v146, v29, v116, -v146
	v_fma_f32 v147, v25, v117, -v147
	v_mul_f32_e64 v150, v25, v136
	v_fma_f32 v150, v29, v137, v150
	v_fma_f32 v150, v116, v142, v150
	v_rcp_f32_e32 v150, v150
	v_cmp_ne_u32_e64 vcc, s37, v16
	v_mul_f32_e64 v150, v150, v22
	v_cndmask_b32_e64 v150, 0, v150, s[30:31]
	v_cndmask_b32_e64 v25, 0, v18, vcc
	v_cndmask_b32_e64 v161, 0, v22, s[30:31]
	v_mul_f32_e64 v103, v136, v150
	v_mul_f32_e64 v156, v137, v150
	v_mul_f32_e64 v157, v142, v150
	v_mul_f32_e64 v158, v143, v150
	v_mul_f32_e64 v159, v146, v150
	v_mul_f32_e64 v160, v147, v150
	v_add_f32_e64 v162, v69, v25
	v_mov_b32_e32 v163, v16
	ds_write_b128 v23, v[100:103]
	ds_write_b128 v23, v[156:159] offset:1024
	ds_write_b128 v23, v[160:163] offset:2048
	v_mov_b32_dpp v62, v92 wave_shr:1 row_mask:0xf bank_mask:0xf bound_ctrl:1
	v_mov_b32_dpp v63, v93 wave_shr:1 row_mask:0xf bank_mask:0xf bound_ctrl:1
	v_mov_b32_dpp v142, v92 wave_shl:1 row_mask:0xf bank_mask:0xf bound_ctrl:1
	v_mov_b32_dpp v143, v93 wave_shl:1 row_mask:0xf bank_mask:0xf bound_ctrl:1
	v_pk_mul_f32 v[44:45], v[92:93], v[104:105] op_sel_hi:[1,0]
	v_pk_mul_f32 v[60:61], v[92:93], v[104:105] op_sel:[0,1]
	v_pk_mul_f32 v[68:69], v[92:93], v[106:107] op_sel_hi:[1,0]
	v_pk_add_f32 v[116:117], v[92:93], v[62:63]
	v_pk_fma_f32 v[44:45], v[62:63], v[76:77], v[44:45] op_sel_hi:[1,0,1]
	v_pk_fma_f32 v[60:61], v[62:63], v[76:77], v[60:61] op_sel:[0,1,0]
	v_pk_fma_f32 v[68:69], v[62:63], v[78:79], v[68:69] op_sel_hi:[1,0,1]
	v_pk_add_f32 v[116:117], v[116:117], v[142:143]
	v_pk_fma_f32 v[44:45], v[142:143], v[80:81], v[44:45] op_sel_hi:[1,0,1]
	v_pk_fma_f32 v[60:61], v[142:143], v[80:81], v[60:61] op_sel:[0,1,0]
	v_pk_fma_f32 v[68:69], v[142:143], v[82:83], v[68:69] op_sel_hi:[1,0,1]
	s_waitcnt lgkmcnt(0)
	s_barrier
	v_pk_add_f32 v[62:63], v[126:127], v[116:117]
	v_pk_add_f32 v[120:121], v[148:149], v[62:63]
	v_pk_add_f32 v[126:127], v[46:47], v[44:45]
	v_pk_add_f32 v[142:143], v[84:85], v[126:127]
	v_pk_add_f32 v[46:47], v[50:51], v[60:61]
	v_pk_add_f32 v[146:147], v[140:141], v[46:47]
	v_pk_add_f32 v[50:51], v[122:123], v[68:69]
	v_pk_add_f32 v[150:151], v[144:145], v[50:51]
	v_pk_fma_f32 v[142:143], v[100:101], v[120:121], v[142:143] op_sel_hi:[0,1,1] neg_lo:[1,0,0] neg_hi:[1,0,0]
	v_pk_fma_f32 v[146:147], v[100:101], v[120:121], v[146:147] op_sel:[1,0,0] neg_lo:[1,0,0] neg_hi:[1,0,0]
	v_pk_fma_f32 v[150:151], v[102:103], v[120:121], v[150:151] op_sel_hi:[0,1,1] neg_lo:[1,0,0] neg_hi:[1,0,0]
	v_pk_mul_f32 v[84:85], v[102:103], v[142:143] op_sel:[1,0]
	v_pk_mul_f32 v[132:133], v[156:157], v[142:143] op_sel_hi:[0,1]
	v_pk_mul_f32 v[136:137], v[156:157], v[142:143] op_sel:[1,0]
	v_pk_fma_f32 v[84:85], v[156:157], v[146:147], v[84:85] op_sel_hi:[0,1,1]
	v_pk_fma_f32 v[132:133], v[158:159], v[146:147], v[132:133] op_sel_hi:[0,1,1]
	v_pk_fma_f32 v[136:137], v[158:159], v[146:147], v[136:137] op_sel:[1,0,0]
	v_pk_fma_f32 v[84:85], v[156:157], v[150:151], v[84:85] op_sel:[1,0,0]
	v_pk_fma_f32 v[132:133], v[158:159], v[150:151], v[132:133] op_sel:[1,0,0]
	v_pk_fma_f32 v[136:137], v[160:161], v[150:151], v[136:137] op_sel_hi:[0,1,1]
	v_pk_mul_f32 v[122:123], v[100:101], v[84:85] op_sel_hi:[0,1]
	v_pk_fma_f32 v[122:123], v[100:101], v[132:133], v[122:123] op_sel:[1,0,0]
	v_pk_fma_f32 v[122:123], v[102:103], v[136:137], v[122:123] op_sel_hi:[0,1,1]
	v_pk_fma_f32 v[122:123], v[160:161], v[120:121], v[122:123] op_sel:[1,0,0] neg_lo:[0,0,1] neg_hi:[0,0,1]
	v_cmp_eq_u32_e64 s[10:11], 6, v163
	v_cmp_eq_u32_e64 s[14:15], 7, v163
	v_pk_add_f32 v[120:121], v[52:53], v[84:85]
	v_pk_add_f32 v[140:141], v[90:91], v[120:121]
	v_pk_add_f32 v[52:53], v[124:125], v[132:133]
	v_pk_add_f32 v[90:91], v[94:95], v[52:53]
	v_pk_add_f32 v[124:125], v[152:153], v[136:137]
	v_pk_add_f32 v[94:95], v[98:99], v[124:125]
	v_pk_add_f32 v[98:99], v[86:87], v[122:123]
	v_pk_add_f32 v[144:145], v[64:65], v[98:99]
	v_pk_fma_f32 v[64:65], v[108:109], v[140:141], v[144:145] op_sel_hi:[0,1,1]
	v_pk_fma_f32 v[148:149], v[112:113], v[140:141], v[144:145] op_sel_hi:[0,1,1]
	v_pk_fma_f32 v[64:65], v[108:109], v[90:91], v[64:65] op_sel:[1,0,0]
	v_pk_fma_f32 v[148:149], v[112:113], v[90:91], v[148:149] op_sel:[1,0,0]
	v_pk_fma_f32 v[64:65], v[110:111], v[94:95], v[64:65] op_sel_hi:[0,1,1]
	v_pk_fma_f32 v[148:149], v[114:115], v[94:95], v[148:149] op_sel_hi:[0,1,1]
	v_pk_fma_f32 v[144:145], v[32:33], v[140:141], v[144:145] op_sel_hi:[0,1,1]
	v_pk_fma_f32 v[144:145], v[32:33], v[90:91], v[144:145] op_sel:[1,0,0]
	v_pk_fma_f32 v[144:145], v[34:35], v[94:95], v[144:145] op_sel_hi:[0,1,1]
	v_cndmask_b32_e64 v86, 0, v18, s[10:11]
	v_cndmask_b32_e64 v87, 0, v18, s[14:15]
	v_add_f32_dpp v144, v64, v144 wave_shl:1 row_mask:0xf bank_mask:0xf bound_ctrl:1
	v_add_f32_dpp v145, v65, v145 wave_shl:1 row_mask:0xf bank_mask:0xf bound_ctrl:1
	s_add_i32 s4, s34, 0
	s_cmpk_lt_i32 s4, 0x201
	s_cselect_b64 s[12:13], s[0:1], 0
	v_add_f32_dpp v144, v148, v144 wave_shr:1 row_mask:0xf bank_mask:0xf bound_ctrl:1
	v_add_f32_dpp v145, v149, v145 wave_shr:1 row_mask:0xf bank_mask:0xf bound_ctrl:1
	v_pk_fma_f32 v[144:145], v[20:21], v[162:163], v[144:145] op_sel_hi:[1,0,1] neg_lo:[0,0,1] neg_hi:[0,0,1]
	v_pk_add_f32 v[144:145], v[144:145], v[86:87] neg_lo:[0,1] neg_hi:[0,1]
	v_pk_mul_f32 v[142:143], v[144:145], v[144:145]
	v_add_f32_e32 v142, v142, v143
	v_cndmask_b32_e64 v143, 0, v142, s[12:13]
	v_add_f32_e32 v1, v1, v143
	s_add_i32 s5, s34, 5
	s_min_i32 s5, s5, 0x200
	s_mul_i32 s6, s5, 0x804
	s_add_i32 s6, s6, s35
	s_add_i32 s7, s6, 0x505014
	s_add_i32 s8, s6, 0x606018
	s_mul_i32 s9, s5, 0x180c
	s_add_i32 s9, s9, s33
	s_add_i32 s4, s34, 6
	s_min_i32 s4, s4, 0x200
	s_mul_i32 s4, s4, 0x804
	s_add_i32 s4, s4, s38
	buffer_load_dword v16, v28, s[20:23], s4 offen nt
	buffer_load_dwordx3 v[32:34], v27, s[24:27], s9 offen nt
	buffer_load_dword v20, v28, s[16:19], s7 offen nt
	buffer_load_dword v21, v28, s[16:19], s8 offen nt
	s_waitcnt vmcnt(8)
	v_mov_b32_dpp v100, v8 wave_shr:1 row_mask:0xf bank_mask:0xf bound_ctrl:1
	v_mov_b32_dpp v101, v9 wave_shr:1 row_mask:0xf bank_mask:0xf bound_ctrl:1
	v_mov_b32_dpp v102, v10 wave_shr:1 row_mask:0xf bank_mask:0xf bound_ctrl:1
	v_mov_b32_dpp v108, v8 wave_shl:1 row_mask:0xf bank_mask:0xf bound_ctrl:1
	v_mov_b32_dpp v109, v9 wave_shl:1 row_mask:0xf bank_mask:0xf bound_ctrl:1
	v_mov_b32_dpp v110, v10 wave_shl:1 row_mask:0xf bank_mask:0xf bound_ctrl:1
	s_add_i32 s4, s34, 4
	s_cmpk_lt_u32 s4, 0x201
	s_cselect_b64 s[12:13], s[40:41], 0
	v_cmp_eq_u32_e64 s[14:15], s37, v2
	s_and_b64 s[14:15], s[14:15], s[12:13]
	v_cndmask_b32_e64 v25, 0, 1, s[14:15]
	v_pk_add_f32 v[64:65], v[8:9], v[100:101]
	v_pk_mul_f32 v[86:87], v[8:9], v[8:9] op_sel_hi:[0,1]
	v_or_b32_dpp v29, v25, v25 wave_shr:1 row_mask:0xf bank_mask:0xf bound_ctrl:1
	v_pk_mul_f32 v[90:91], v[8:9], v[10:11] op_sel_hi:[1,0]
	v_or_b32_dpp v29, v25, v29 wave_shl:1 row_mask:0xf bank_mask:0xf bound_ctrl:1
	v_mul_f32_e64 v94, v9, v9
	v_mul_f32_e64 v95, v10, v10
	v_or_b32_dpp v56, v29, v29 wave_shr:1 row_mask:0xf bank_mask:0xf bound_ctrl:1
	v_add_f32_e64 v112, v10, v102
	v_pk_add_f32 v[64:65], v[64:65], v[108:109]
	v_or_b32_dpp v56, v29, v56 wave_shl:1 row_mask:0xf bank_mask:0xf bound_ctrl:1
	v_or3_b32 v25, v56, v30, v57
	v_or3_b32 v25, v25, v88, v89
	s_add_i32 s4, s34, 1
	s_cmpk_lt_u32 s4, 0x1ff
	s_cselect_b64 s[12:13], s[42:43], 0
	v_cmp_ne_u32_e64 s[30:31], 0, v25
	s_and_b64 s[30:31], s[30:31], s[12:13]
	v_cndmask_b32_e64 v25, 0, 1.0, s[30:31]
	v_pk_fma_f32 v[86:87], v[100:101], v[100:101], v[86:87] op_sel_hi:[0,1,1]
	v_pk_fma_f32 v[90:91], v[100:101], v[102:103], v[90:91] op_sel_hi:[1,0,1]
	v_fma_f32 v94, v101, v101, v94
	v_fma_f32 v95, v102, v102, v95
	v_add_f32_dpp v113, v25, v25 wave_shr:1 row_mask:0xf bank_mask:0xf bound_ctrl:1
	v_add_f32_e64 v112, v112, v110
	v_pk_fma_f32 v[86:87], v[108:109], v[108:109], v[86:87] op_sel_hi:[0,1,1]
	v_pk_fma_f32 v[90:91], v[108:109], v[110:111], v[90:91] op_sel_hi:[1,0,1]
	v_fma_f32 v94, v109, v109, v94
	v_fma_f32 v95, v110, v110, v95
	v_add_f32_dpp v113, v25, v113 wave_shl:1 row_mask:0xf bank_mask:0xf bound_ctrl:1
	v_pk_add_f32 v[114:115], v[130:131], v[64:65]
	v_pk_add_f32 v[130:131], v[134:135], v[86:87]
	v_pk_add_f32 v[134:135], v[138:139], v[90:91]
	v_pk_add_f32 v[138:139], v[96:97], v[94:95]
	v_pk_add_f32 v[96:97], v[118:119], v[112:113]
	v_mul_f32_e64 v140, v114, v22
	v_mul_f32_e64 v141, v115, v22
	v_mul_f32_e64 v142, v96, v22
	v_fma_f32 v25, v130, v22, v26
	v_mul_f32_e64 v29, v131, v22
	v_mul_f32_e64 v118, v134, v22
	v_fma_f32 v119, v138, v22, v26
	v_mul_f32_e64 v152, v135, v22
	v_fma_f32 v153, v139, v22, v26
	v_fma_f32 v25, -v140, v140, v25
	v_fma_f32 v29, -v140, v141, v29
	v_fma_f32 v118, -v140, v142, v118
	v_fma_f32 v119, -v141, v141, v119
	v_fma_f32 v152, -v141, v142, v152
	v_fma_f32 v153, -v142, v142, v153
	v_mul_f32_e64 v154, v152, v152
	v_mul_f32_e64 v155, v29, v153
	v_mul_f32_e64 v156, v118, v119
	v_mul_f32_e64 v157, v118, v118
	v_mul_f32_e64 v158, v25, v152
	v_mul_f32_e64 v159, v29, v29
	v_fma_f32 v154, v119, v153, -v154
	v_fma_f32 v155, v118, v152, -v155
	v_fma_f32 v156, v29, v152, -v156
	v_fma_f32 v157, v25, v153, -v157
	v_fma_f32 v158, v29, v118, -v158
	v_fma_f32 v159, v25, v119, -v159
	v_mul_f32_e64 v160, v25, v154
	v_fma_f32 v160, v29, v155, v160
	v_fma_f32 v160, v118, v156, v160
	v_rcp_f32_e32 v160, v160
	v_cmp_ne_u32_e64 vcc, s37, v31
	v_mul_f32_e64 v160, v160, v22
	v_cndmask_b32_e64 v160, 0, v160, s[30:31]
	v_cndmask_b32_e64 v25, 0, v18, vcc
	v_cndmask_b32_e64 v149, 0, v22, s[30:31]
	v_mul_f32_e64 v143, v154, v160
	v_mul_f32_e64 v144, v155, v160
	v_mul_f32_e64 v145, v156, v160
	v_mul_f32_e64 v146, v157, v160
	v_mul_f32_e64 v147, v158, v160
	v_mul_f32_e64 v148, v159, v160
	v_add_f32_e64 v150, v97, v25
	v_mov_b32_e32 v151, v31
	ds_write_b128 v23, v[140:143] offset:3072
	ds_write_b128 v23, v[144:147] offset:4096
	ds_write_b128 v23, v[148:151] offset:5120
	v_mov_b32_dpp v114, v4 wave_shr:1 row_mask:0xf bank_mask:0xf bound_ctrl:1
	v_mov_b32_dpp v115, v5 wave_shr:1 row_mask:0xf bank_mask:0xf bound_ctrl:1
	v_mov_b32_dpp v118, v4 wave_shl:1 row_mask:0xf bank_mask:0xf bound_ctrl:1
	v_mov_b32_dpp v119, v5 wave_shl:1 row_mask:0xf bank_mask:0xf bound_ctrl:1
	v_pk_mul_f32 v[96:97], v[4:5], v[8:9] op_sel_hi:[1,0]
	v_pk_mul_f32 v[152:153], v[4:5], v[8:9] op_sel:[0,1]
	v_pk_mul_f32 v[156:157], v[4:5], v[10:11] op_sel_hi:[1,0]
	v_pk_add_f32 v[160:161], v[4:5], v[114:115]
	v_pk_fma_f32 v[96:97], v[114:115], v[100:101], v[96:97] op_sel_hi:[1,0,1]
	v_pk_fma_f32 v[152:153], v[114:115], v[100:101], v[152:153] op_sel:[0,1,0]
	v_pk_fma_f32 v[156:157], v[114:115], v[102:103], v[156:157] op_sel_hi:[1,0,1]
	v_pk_add_f32 v[160:161], v[160:161], v[118:119]
	v_pk_fma_f32 v[96:97], v[118:119], v[108:109], v[96:97] op_sel_hi:[1,0,1]
	v_pk_fma_f32 v[152:153], v[118:119], v[108:109], v[152:153] op_sel:[0,1,0]
	v_pk_fma_f32 v[156:157], v[118:119], v[110:111], v[156:157] op_sel_hi:[1,0,1]
	s_waitcnt lgkmcnt(0)
	s_barrier
	v_pk_add_f32 v[114:115], v[62:63], v[160:161]
	v_pk_add_f32 v[164:165], v[126:127], v[96:97]
	v_pk_add_f32 v[168:169], v[46:47], v[152:153]
	v_pk_add_f32 v[172:173], v[50:51], v[156:157]
	v_pk_fma_f32 v[164:165], v[140:141], v[114:115], v[164:165] op_sel_hi:[0,1,1] neg_lo:[1,0,0] neg_hi:[1,0,0]
	v_pk_fma_f32 v[168:169], v[140:141], v[114:115], v[168:169] op_sel:[1,0,0] neg_lo:[1,0,0] neg_hi:[1,0,0]
	v_pk_fma_f32 v[172:173], v[142:143], v[114:115], v[172:173] op_sel_hi:[0,1,1] neg_lo:[1,0,0] neg_hi:[1,0,0]
	v_pk_mul_f32 v[46:47], v[142:143], v[164:165] op_sel:[1,0]
	v_pk_mul_f32 v[50:51], v[144:145], v[164:165] op_sel_hi:[0,1]
	v_pk_mul_f32 v[62:63], v[144:145], v[164:165] op_sel:[1,0]
	v_pk_fma_f32 v[46:47], v[144:145], v[168:169], v[46:47] op_sel_hi:[0,1,1]
	v_pk_fma_f32 v[50:51], v[146:147], v[168:169], v[50:51] op_sel_hi:[0,1,1]
	v_pk_fma_f32 v[62:63], v[146:147], v[168:169], v[62:63] op_sel:[1,0,0]
	v_pk_fma_f32 v[46:47], v[144:145], v[172:173], v[46:47] op_sel:[1,0,0]
	v_pk_fma_f32 v[50:51], v[146:147], v[172:173], v[50:51] op_sel:[1,0,0]
	v_pk_fma_f32 v[62:63], v[148:149], v[172:173], v[62:63] op_sel_hi:[0,1,1]
	v_pk_mul_f32 v[176:177], v[140:141], v[46:47] op_sel_hi:[0,1]
	v_pk_fma_f32 v[176:177], v[140:141], v[50:51], v[176:177] op_sel:[1,0,0]
	v_pk_fma_f32 v[176:177], v[142:143], v[62:63], v[176:177] op_sel_hi:[0,1,1]
	v_pk_fma_f32 v[176:177], v[148:149], v[114:115], v[176:177] op_sel:[1,0,0] neg_lo:[0,0,1] neg_hi:[0,0,1]
	v_cmp_eq_u32_e64 s[10:11], 6, v151
	v_cmp_eq_u32_e64 s[14:15], 7, v151
	v_pk_add_f32 v[114:115], v[120:121], v[46:47]
	v_pk_add_f32 v[118:119], v[52:53], v[50:51]
	v_pk_add_f32 v[52:53], v[124:125], v[62:63]
	v_pk_add_f32 v[120:121], v[98:99], v[176:177]
	v_pk_fma_f32 v[124:125], v[36:37], v[114:115], v[120:121] op_sel_hi:[0,1,1]
	v_pk_fma_f32 v[164:165], v[40:41], v[114:115], v[120:121] op_sel_hi:[0,1,1]
	v_pk_fma_f32 v[124:125], v[36:37], v[118:119], v[124:125] op_sel:[1,0,0]
	v_pk_fma_f32 v[164:165], v[40:41], v[118:119], v[164:165] op_sel:[1,0,0]
	v_pk_fma_f32 v[124:125], v[38:39], v[52:53], v[124:125] op_sel_hi:[0,1,1]
	v_pk_fma_f32 v[164:165], v[42:43], v[52:53], v[164:165] op_sel_hi:[0,1,1]
	v_pk_fma_f32 v[120:121], v[72:73], v[114:115], v[120:121] op_sel_hi:[0,1,1]
	v_pk_fma_f32 v[120:121], v[72:73], v[118:119], v[120:121] op_sel:[1,0,0]
	v_pk_fma_f32 v[120:121], v[74:75], v[52:53], v[120:121] op_sel_hi:[0,1,1]
	v_cndmask_b32_e64 v98, 0, v18, s[10:11]
	v_cndmask_b32_e64 v99, 0, v18, s[14:15]
	v_add_f32_dpp v120, v124, v120 wave_shl:1 row_mask:0xf bank_mask:0xf bound_ctrl:1
	v_add_f32_dpp v121, v125, v121 wave_shl:1 row_mask:0xf bank_mask:0xf bound_ctrl:1
	s_add_i32 s4, s34, 1
	s_cmpk_lt_i32 s4, 0x201
	s_cselect_b64 s[12:13], s[0:1], 0
	v_add_f32_dpp v120, v164, v120 wave_shr:1 row_mask:0xf bank_mask:0xf bound_ctrl:1
	v_add_f32_dpp v121, v165, v121 wave_shr:1 row_mask:0xf bank_mask:0xf bound_ctrl:1
	v_pk_fma_f32 v[120:121], v[58:59], v[150:151], v[120:121] op_sel_hi:[1,0,1] neg_lo:[0,0,1] neg_hi:[0,0,1]
	v_pk_add_f32 v[120:121], v[120:121], v[98:99] neg_lo:[0,1] neg_hi:[0,1]
	v_pk_mul_f32 v[126:127], v[120:121], v[120:121]
	v_add_f32_e32 v126, v126, v127
	v_cndmask_b32_e64 v127, 0, v126, s[12:13]
	v_add_f32_e32 v1, v1, v127
	s_add_i32 s5, s34, 6
	s_min_i32 s5, s5, 0x200
	s_mul_i32 s6, s5, 0x804
	s_add_i32 s6, s6, s35
	s_add_i32 s7, s6, 0x505014
	s_add_i32 s8, s6, 0x606018
	s_mul_i32 s9, s5, 0x180c
	s_add_i32 s9, s9, s33
	s_add_i32 s4, s34, 7
	s_min_i32 s4, s4, 0x200
	s_mul_i32 s4, s4, 0x804
	s_add_i32 s4, s4, s38
	buffer_load_dword v25, v28, s[20:23], s4 offen nt
	buffer_load_dwordx3 v[40:42], v27, s[24:27], s9 offen nt
	buffer_load_dword v36, v28, s[16:19], s7 offen nt
	buffer_load_dword v37, v28, s[16:19], s8 offen nt
	s_waitcnt vmcnt(8)
	v_mov_b32_dpp v72, v12 wave_shr:1 row_mask:0xf bank_mask:0xf bound_ctrl:1
	v_mov_b32_dpp v73, v13 wave_shr:1 row_mask:0xf bank_mask:0xf bound_ctrl:1
	v_mov_b32_dpp v74, v14 wave_shr:1 row_mask:0xf bank_mask:0xf bound_ctrl:1
	v_mov_b32_dpp v124, v12 wave_shl:1 row_mask:0xf bank_mask:0xf bound_ctrl:1
	v_mov_b32_dpp v125, v13 wave_shl:1 row_mask:0xf bank_mask:0xf bound_ctrl:1
	v_mov_b32_dpp v126, v14 wave_shl:1 row_mask:0xf bank_mask:0xf bound_ctrl:1
	s_add_i32 s4, s34, 5
	s_cmpk_lt_u32 s4, 0x201
	s_cselect_b64 s[12:13], s[40:41], 0
	v_cmp_eq_u32_e64 s[14:15], s37, v3
	s_and_b64 s[14:15], s[14:15], s[12:13]
	v_cndmask_b32_e64 v29, 0, 1, s[14:15]
	v_pk_add_f32 v[38:39], v[12:13], v[72:73]
	v_pk_mul_f32 v[52:53], v[12:13], v[12:13] op_sel_hi:[0,1]
	v_or_b32_dpp v31, v29, v29 wave_shr:1 row_mask:0xf bank_mask:0xf bound_ctrl:1
	v_pk_mul_f32 v[58:59], v[12:13], v[14:15] op_sel_hi:[1,0]
	v_or_b32_dpp v31, v29, v31 wave_shl:1 row_mask:0xf bank_mask:0xf bound_ctrl:1
	v_mul_f32_e64 v98, v13, v13
	v_mul_f32_e64 v99, v14, v14
	v_or_b32_dpp v89, v31, v31 wave_shr:1 row_mask:0xf bank_mask:0xf bound_ctrl:1
	v_add_f32_e64 v114, v14, v74
	v_pk_add_f32 v[38:39], v[38:39], v[124:125]
	v_or_b32_dpp v89, v31, v89 wave_shl:1 row_mask:0xf bank_mask:0xf bound_ctrl:1
	v_or3_b32 v29, v89, v56, v30
	v_or3_b32 v29, v29, v57, v88
	s_add_i32 s4, s34, 2
	s_cmpk_lt_u32 s4, 0x1ff
	s_cselect_b64 s[12:13], s[42:43], 0
	v_cmp_ne_u32_e64 s[30:31], 0, v29
	s_and_b64 s[30:31], s[30:31], s[12:13]
	v_cndmask_b32_e64 v29, 0, 1.0, s[30:31]
	v_pk_fma_f32 v[52:53], v[72:73], v[72:73], v[52:53] op_sel_hi:[0,1,1]
	v_pk_fma_f32 v[58:59], v[72:73], v[74:75], v[58:59] op_sel_hi:[1,0,1]
	v_fma_f32 v98, v73, v73, v98
	v_fma_f32 v99, v74, v74, v99
	v_add_f32_dpp v115, v29, v29 wave_shr:1 row_mask:0xf bank_mask:0xf bound_ctrl:1
	v_add_f32_e64 v114, v114, v126
	v_pk_fma_f32 v[52:53], v[124:125], v[124:125], v[52:53] op_sel_hi:[0,1,1]
	v_pk_fma_f32 v[58:59], v[124:125], v[126:127], v[58:59] op_sel_hi:[1,0,1]
	v_fma_f32 v98, v125, v125, v98
	v_fma_f32 v99, v126, v126, v99
	v_add_f32_dpp v115, v29, v115 wave_shl:1 row_mask:0xf bank_mask:0xf bound_ctrl:1
	v_pk_add_f32 v[118:119], v[64:65], v[38:39]
	v_pk_add_f32 v[120:121], v[48:49], v[118:119]
	v_pk_add_f32 v[48:49], v[86:87], v[52:53]
	v_pk_add_f32 v[64:65], v[54:55], v[48:49]
	v_pk_add_f32 v[140:141], v[90:91], v[58:59]
	v_pk_add_f32 v[54:55], v[66:67], v[140:141]
	v_pk_add_f32 v[144:145], v[94:95], v[98:99]
	v_pk_add_f32 v[66:67], v[70:71], v[144:145]
	v_pk_add_f32 v[70:71], v[112:113], v[114:115]
	v_pk_add_f32 v[86:87], v[128:129], v[70:71]
	v_mul_f32_e64 v128, v120, v22
	v_mul_f32_e64 v129, v121, v22
	v_mul_f32_e64 v130, v86, v22
	v_fma_f32 v29, v64, v22, v26
	v_mul_f32_e64 v31, v65, v22
	v_mul_f32_e64 v90, v54, v22
	v_fma_f32 v91, v66, v22, v26
	v_mul_f32_e64 v94, v55, v22
	v_fma_f32 v95, v67, v22, v26
	v_fma_f32 v29, -v128, v128, v29
	v_fma_f32 v31, -v128, v129, v31
	v_fma_f32 v90, -v128, v130, v90
	v_fma_f32 v91, -v129, v129, v91
	v_fma_f32 v94, -v129, v130, v94
	v_fma_f32 v95, -v130, v130, v95
	v_mul_f32_e64 v112, v94, v94
	v_mul_f32_e64 v113, v31, v95
	v_mul_f32_e64 v134, v90, v91
	v_mul_f32_e64 v135, v90, v90
	v_mul_f32_e64 v138, v29, v94
	v_mul_f32_e64 v139, v31, v31
	v_fma_f32 v112, v91, v95, -v112
	v_fma_f32 v113, v90, v94, -v113
	v_fma_f32 v134, v31, v94, -v134
	v_fma_f32 v135, v29, v95, -v135
	v_fma_f32 v138, v31, v90, -v138
	v_fma_f32 v139, v29, v91, -v139
	v_mul_f32_e64 v142, v29, v112
	v_fma_f32 v142, v31, v113, v142
	v_fma_f32 v142, v90, v134, v142
	v_rcp_f32_e32 v142, v142
	v_cmp_ne_u32_e64 vcc, s37, v24
	v_mul_f32_e64 v142, v142, v22
	v_cndmask_b32_e64 v142, 0, v142, s[30:31]
	v_cndmask_b32_e64 v29, 0, v18, vcc
	v_cndmask_b32_e64 v165, 0, v22, s[30:31]
	v_mul_f32_e64 v131, v112, v142
	v_mul_f32_e64 v148, v113, v142
	v_mul_f32_e64 v149, v134, v142
	v_mul_f32_e64 v150, v135, v142
	v_mul_f32_e64 v151, v138, v142
	v_mul_f32_e64 v164, v139, v142
	v_add_f32_e64 v166, v87, v29
	v_mov_b32_e32 v167, v24
	ds_write_b128 v23, v[128:131]
	ds_write_b128 v23, v[148:151] offset:1024
	ds_write_b128 v23, v[164:167] offset:2048
	v_mov_b32_dpp v64, v6 wave_shr:1 row_mask:0xf bank_mask:0xf bound_ctrl:1
	v_mov_b32_dpp v65, v7 wave_shr:1 row_mask:0xf bank_mask:0xf bound_ctrl:1
	v_mov_b32_dpp v112, v6 wave_shl:1 row_mask:0xf bank_mask:0xf bound_ctrl:1
	v_mov_b32_dpp v113, v7 wave_shl:1 row_mask:0xf bank_mask:0xf bound_ctrl:1
	v_pk_mul_f32 v[54:55], v[6:7], v[12:13] op_sel_hi:[1,0]
	v_pk_mul_f32 v[66:67], v[6:7], v[12:13] op_sel:[0,1]
	v_pk_mul_f32 v[86:87], v[6:7], v[14:15] op_sel_hi:[1,0]
	v_pk_add_f32 v[90:91], v[6:7], v[64:65]
	v_pk_fma_f32 v[54:55], v[64:65], v[72:73], v[54:55] op_sel_hi:[1,0,1]
	v_pk_fma_f32 v[66:67], v[64:65], v[72:73], v[66:67] op_sel:[0,1,0]
	v_pk_fma_f32 v[86:87], v[64:65], v[74:75], v[86:87] op_sel_hi:[1,0,1]
	v_pk_add_f32 v[90:91], v[90:91], v[112:113]
	v_pk_fma_f32 v[54:55], v[112:113], v[124:125], v[54:55] op_sel_hi:[1,0,1]
	v_pk_fma_f32 v[66:67], v[112:113], v[124:125], v[66:67] op_sel:[0,1,0]
	v_pk_fma_f32 v[86:87], v[112:113], v[126:127], v[86:87] op_sel_hi:[1,0,1]
	s_waitcnt lgkmcnt(0)
	s_barrier
	v_pk_add_f32 v[94:95], v[160:161], v[90:91]
	v_pk_add_f32 v[64:65], v[116:117], v[94:95]
	v_pk_add_f32 v[134:135], v[96:97], v[54:55]
	v_pk_add_f32 v[138:139], v[44:45], v[134:135]
	v_pk_add_f32 v[142:143], v[152:153], v[66:67]
	v_pk_add_f32 v[146:147], v[60:61], v[142:143]
	v_pk_add_f32 v[154:155], v[156:157], v[86:87]
	v_pk_add_f32 v[158:159], v[68:69], v[154:155]
	v_pk_fma_f32 v[138:139], v[128:129], v[64:65], v[138:139] op_sel_hi:[0,1,1] neg_lo:[1,0,0] neg_hi:[1,0,0]
	v_pk_fma_f32 v[146:147], v[128:129], v[64:65], v[146:147] op_sel:[1,0,0] neg_lo:[1,0,0] neg_hi:[1,0,0]
	v_pk_fma_f32 v[158:159], v[130:131], v[64:65], v[158:159] op_sel_hi:[0,1,1] neg_lo:[1,0,0] neg_hi:[1,0,0]
	v_pk_mul_f32 v[44:45], v[130:131], v[138:139] op_sel:[1,0]
	v_pk_mul_f32 v[60:61], v[148:149], v[138:139] op_sel_hi:[0,1]
	v_pk_mul_f32 v[68:69], v[148:149], v[138:139] op_sel:[1,0]
	v_pk_fma_f32 v[44:45], v[148:149], v[146:147], v[44:45] op_sel_hi:[0,1,1]
	v_pk_fma_f32 v[60:61], v[150:151], v[146:147], v[60:61] op_sel_hi:[0,1,1]
	v_pk_fma_f32 v[68:69], v[150:151], v[146:147], v[68:69] op_sel:[1,0,0]
	v_pk_fma_f32 v[44:45], v[148:149], v[158:159], v[44:45] op_sel:[1,0,0]
	v_pk_fma_f32 v[60:61], v[150:151], v[158:159], v[60:61] op_sel:[1,0,0]
	v_pk_fma_f32 v[68:69], v[164:165], v[158:159], v[68:69] op_sel_hi:[0,1,1]
	v_pk_mul_f32 v[162:163], v[128:129], v[44:45] op_sel_hi:[0,1]
	v_pk_fma_f32 v[162:163], v[128:129], v[60:61], v[162:163] op_sel:[1,0,0]
	v_pk_fma_f32 v[162:163], v[130:131], v[68:69], v[162:163] op_sel_hi:[0,1,1]
	v_pk_fma_f32 v[162:163], v[164:165], v[64:65], v[162:163] op_sel:[1,0,0] neg_lo:[0,0,1] neg_hi:[0,0,1]
	v_cmp_eq_u32_e64 s[10:11], 6, v167
	v_cmp_eq_u32_e64 s[14:15], 7, v167
	v_pk_add_f32 v[138:139], v[46:47], v[44:45]
	v_pk_add_f32 v[64:65], v[84:85], v[138:139]
	v_pk_add_f32 v[46:47], v[50:51], v[60:61]
	v_pk_add_f32 v[84:85], v[132:133], v[46:47]
	v_pk_add_f32 v[50:51], v[62:63], v[68:69]
	v_pk_add_f32 v[96:97], v[136:137], v[50:51]
	v_pk_add_f32 v[112:113], v[176:177], v[162:163]
	v_pk_add_f32 v[62:63], v[122:123], v[112:113]
	v_pk_fma_f32 v[122:123], v[76:77], v[64:65], v[62:63] op_sel_hi:[0,1,1]
	v_pk_fma_f32 v[146:147], v[80:81], v[64:65], v[62:63] op_sel_hi:[0,1,1]
	v_pk_fma_f32 v[122:123], v[76:77], v[84:85], v[122:123] op_sel:[1,0,0]
	v_pk_fma_f32 v[146:147], v[80:81], v[84:85], v[146:147] op_sel:[1,0,0]
	v_pk_fma_f32 v[122:123], v[78:79], v[96:97], v[122:123] op_sel_hi:[0,1,1]
	v_pk_fma_f32 v[146:147], v[82:83], v[96:97], v[146:147] op_sel_hi:[0,1,1]
	v_pk_fma_f32 v[62:63], v[104:105], v[64:65], v[62:63] op_sel_hi:[0,1,1]
	v_pk_fma_f32 v[62:63], v[104:105], v[84:85], v[62:63] op_sel:[1,0,0]
	v_pk_fma_f32 v[62:63], v[106:107], v[96:97], v[62:63] op_sel_hi:[0,1,1]
	v_cndmask_b32_e64 v116, 0, v18, s[10:11]
	v_cndmask_b32_e64 v117, 0, v18, s[14:15]
	v_add_f32_dpp v62, v122, v62 wave_shl:1 row_mask:0xf bank_mask:0xf bound_ctrl:1
	v_add_f32_dpp v63, v123, v63 wave_shl:1 row_mask:0xf bank_mask:0xf bound_ctrl:1
	s_add_i32 s4, s34, 2
	s_cmpk_lt_i32 s4, 0x201
	s_cselect_b64 s[12:13], s[0:1], 0
	v_add_f32_dpp v62, v146, v62 wave_shr:1 row_mask:0xf bank_mask:0xf bound_ctrl:1
	v_add_f32_dpp v63, v147, v63 wave_shr:1 row_mask:0xf bank_mask:0xf bound_ctrl:1
	v_pk_fma_f32 v[62:63], v[92:93], v[166:167], v[62:63] op_sel_hi:[1,0,1] neg_lo:[0,0,1] neg_hi:[0,0,1]
	v_pk_add_f32 v[62:63], v[62:63], v[116:117] neg_lo:[0,1] neg_hi:[0,1]
	v_pk_mul_f32 v[120:121], v[62:63], v[62:63]
	v_add_f32_e32 v120, v120, v121
	v_cndmask_b32_e64 v121, 0, v120, s[12:13]
	v_add_f32_e32 v1, v1, v121
	s_add_i32 s5, s34, 7
	s_min_i32 s5, s5, 0x200
	s_mul_i32 s6, s5, 0x804
	s_add_i32 s6, s6, s35
	s_add_i32 s7, s6, 0x505014
	s_add_i32 s8, s6, 0x606018
	s_mul_i32 s9, s5, 0x180c
	s_add_i32 s9, s9, s33
	s_add_i32 s4, s34, 8
	s_min_i32 s4, s4, 0x200
	s_mul_i32 s4, s4, 0x804
	s_add_i32 s4, s4, s38
	buffer_load_dword v24, v28, s[20:23], s4 offen nt
	buffer_load_dwordx3 v[76:78], v27, s[24:27], s9 offen nt
	buffer_load_dword v62, v28, s[16:19], s7 offen nt
	buffer_load_dword v63, v28, s[16:19], s8 offen nt
	s_waitcnt vmcnt(8)
	v_mov_b32_dpp v80, v32 wave_shr:1 row_mask:0xf bank_mask:0xf bound_ctrl:1
	v_mov_b32_dpp v81, v33 wave_shr:1 row_mask:0xf bank_mask:0xf bound_ctrl:1
	v_mov_b32_dpp v82, v34 wave_shr:1 row_mask:0xf bank_mask:0xf bound_ctrl:1
	v_mov_b32_dpp v104, v32 wave_shl:1 row_mask:0xf bank_mask:0xf bound_ctrl:1
	v_mov_b32_dpp v105, v33 wave_shl:1 row_mask:0xf bank_mask:0xf bound_ctrl:1
	v_mov_b32_dpp v106, v34 wave_shl:1 row_mask:0xf bank_mask:0xf bound_ctrl:1
	s_add_i32 s4, s34, 6
	s_cmpk_lt_u32 s4, 0x201
	s_cselect_b64 s[12:13], s[40:41], 0
	v_cmp_eq_u32_e64 s[14:15], s37, v16
	s_and_b64 s[14:15], s[14:15], s[12:13]
	v_cndmask_b32_e64 v29, 0, 1, s[14:15]
	v_pk_add_f32 v[64:65], v[32:33], v[80:81]
	v_pk_mul_f32 v[84:85], v[32:33], v[32:33] op_sel_hi:[0,1]
	v_or_b32_dpp v31, v29, v29 wave_shr:1 row_mask:0xf bank_mask:0xf bound_ctrl:1
	v_pk_mul_f32 v[92:93], v[32:33], v[34:35] op_sel_hi:[1,0]
	v_or_b32_dpp v31, v29, v31 wave_shl:1 row_mask:0xf bank_mask:0xf bound_ctrl:1
	v_mul_f32_e64 v96, v33, v33
	v_mul_f32_e64 v97, v34, v34
	v_or_b32_dpp v88, v31, v31 wave_shr:1 row_mask:0xf bank_mask:0xf bound_ctrl:1
	v_add_f32_e64 v116, v34, v82
	v_pk_add_f32 v[64:65], v[64:65], v[104:105]
	v_or_b32_dpp v88, v31, v88 wave_shl:1 row_mask:0xf bank_mask:0xf bound_ctrl:1
	v_or3_b32 v29, v88, v89, v56
	v_or3_b32 v29, v29, v30, v57
	s_add_i32 s4, s34, 3
	s_cmpk_lt_u32 s4, 0x1ff
	s_cselect_b64 s[12:13], s[42:43], 0
	v_cmp_ne_u32_e64 s[30:31], 0, v29
	s_and_b64 s[30:31], s[30:31], s[12:13]
	v_cndmask_b32_e64 v29, 0, 1.0, s[30:31]
	v_pk_fma_f32 v[84:85], v[80:81], v[80:81], v[84:85] op_sel_hi:[0,1,1]
	v_pk_fma_f32 v[92:93], v[80:81], v[82:83], v[92:93] op_sel_hi:[1,0,1]
	v_fma_f32 v96, v81, v81, v96
	v_fma_f32 v97, v82, v82, v97
	v_add_f32_dpp v117, v29, v29 wave_shr:1 row_mask:0xf bank_mask:0xf bound_ctrl:1
	v_add_f32_e64 v116, v116, v106
	v_pk_fma_f32 v[84:85], v[104:105], v[104:105], v[84:85] op_sel_hi:[0,1,1]
	v_pk_fma_f32 v[92:93], v[104:105], v[106:107], v[92:93] op_sel_hi:[1,0,1]
	v_fma_f32 v96, v105, v105, v96
	v_fma_f32 v97, v106, v106, v97
	v_add_f32_dpp v117, v29, v117 wave_shl:1 row_mask:0xf bank_mask:0xf bound_ctrl:1
	v_pk_add_f32 v[120:121], v[118:119], v[64:65]
	v_pk_add_f32 v[118:119], v[48:49], v[84:85]
	v_pk_add_f32 v[48:49], v[140:141], v[92:93]
	v_pk_add_f32 v[122:123], v[144:145], v[96:97]
	v_pk_add_f32 v[128:129], v[70:71], v[116:117]
	v_mul_f32_e64 v144, v120, v22
	v_mul_f32_e64 v145, v121, v22
	v_mul_f32_e64 v146, v128, v22
	v_fma_f32 v29, v118, v22, v26
	v_mul_f32_e64 v31, v119, v22
	v_mul_f32_e64 v70, v48, v22
	v_fma_f32 v71, v122, v22, v26
	v_mul_f32_e64 v130, v49, v22
	v_fma_f32 v131, v123, v22, v26
	v_fma_f32 v29, -v144, v144, v29
	v_fma_f32 v31, -v144, v145, v31
	v_fma_f32 v70, -v144, v146, v70
	v_fma_f32 v71, -v145, v145, v71
	v_fma_f32 v130, -v145, v146, v130
	v_fma_f32 v131, -v146, v146, v131
	v_mul_f32_e64 v132, v130, v130
	v_mul_f32_e64 v133, v31, v131
	v_mul_f32_e64 v136, v70, v71
	v_mul_f32_e64 v137, v70, v70
	v_mul_f32_e64 v140, v29, v130
	v_mul_f32_e64 v141, v31, v31
	v_fma_f32 v132, v71, v131, -v132
	v_fma_f32 v133, v70, v130, -v133
	v_fma_f32 v136, v31, v130, -v136
	v_fma_f32 v137, v29, v131, -v137
	v_fma_f32 v140, v31, v70, -v140
	v_fma_f32 v141, v29, v71, -v141
	v_mul_f32_e64 v152, v29, v132
	v_fma_f32 v152, v31, v133, v152
	v_fma_f32 v152, v70, v136, v152
	v_rcp_f32_e32 v152, v152
	v_cmp_ne_u32_e64 vcc, s37, v17
	v_mul_f32_e64 v152, v152, v22
	v_cndmask_b32_e64 v152, 0, v152, s[30:31]
	v_cndmask_b32_e64 v29, 0, v18, vcc
	v_cndmask_b32_e64 v157, 0, v22, s[30:31]
	v_mul_f32_e64 v147, v132, v152
	v_mul_f32_e64 v148, v133, v152
	v_mul_f32_e64 v149, v136, v152
	v_mul_f32_e64 v150, v137, v152
	v_mul_f32_e64 v151, v140, v152
	v_mul_f32_e64 v156, v141, v152
	v_add_f32_e64 v158, v129, v29
	v_mov_b32_e32 v159, v17
	ds_write_b128 v23, v[144:147] offset:3072
	ds_write_b128 v23, v[148:151] offset:4096
	ds_write_b128 v23, v[156:159] offset:5120
	v_mov_b32_dpp v70, v20 wave_shr:1 row_mask:0xf bank_mask:0xf bound_ctrl:1
	v_mov_b32_dpp v71, v21 wave_shr:1 row_mask:0xf bank_mask:0xf bound_ctrl:1
	v_mov_b32_dpp v118, v20 wave_shl:1 row_mask:0xf bank_mask:0xf bound_ctrl:1
	v_mov_b32_dpp v119, v21 wave_shl:1 row_mask:0xf bank_mask:0xf bound_ctrl:1
	v_pk_mul_f32 v[48:49], v[20:21], v[32:33] op_sel_hi:[1,0]
	v_pk_mul_f32 v[120:121], v[20:21], v[32:33] op_sel:[0,1]
	v_pk_mul_f32 v[128:129], v[20:21], v[34:35] op_sel_hi:[1,0]
	v_pk_add_f32 v[132:133], v[20:21], v[70:71]
	v_pk_fma_f32 v[48:49], v[70:71], v[80:81], v[48:49] op_sel_hi:[1,0,1]
	v_pk_fma_f32 v[120:121], v[70:71], v[80:81], v[120:121] op_sel:[0,1,0]
	v_pk_fma_f32 v[128:129], v[70:71], v[82:83], v[128:129] op_sel_hi:[1,0,1]
	v_pk_add_f32 v[132:133], v[132:133], v[118:119]
	v_pk_fma_f32 v[48:49], v[118:119], v[104:105], v[48:49] op_sel_hi:[1,0,1]
	v_pk_fma_f32 v[120:121], v[118:119], v[104:105], v[120:121] op_sel:[0,1,0]
	v_pk_fma_f32 v[128:129], v[118:119], v[106:107], v[128:129] op_sel_hi:[1,0,1]
	s_waitcnt lgkmcnt(0)
	s_barrier
	v_pk_add_f32 v[70:71], v[94:95], v[132:133]
	v_pk_add_f32 v[136:137], v[134:135], v[48:49]
	v_pk_add_f32 v[140:141], v[142:143], v[120:121]
	v_pk_add_f32 v[152:153], v[154:155], v[128:129]
	v_pk_fma_f32 v[136:137], v[144:145], v[70:71], v[136:137] op_sel_hi:[0,1,1] neg_lo:[1,0,0] neg_hi:[1,0,0]
	v_pk_fma_f32 v[140:141], v[144:145], v[70:71], v[140:141] op_sel:[1,0,0] neg_lo:[1,0,0] neg_hi:[1,0,0]
	v_pk_fma_f32 v[152:153], v[146:147], v[70:71], v[152:153] op_sel_hi:[0,1,1] neg_lo:[1,0,0] neg_hi:[1,0,0]
	v_pk_mul_f32 v[94:95], v[146:147], v[136:137] op_sel:[1,0]
	v_pk_mul_f32 v[118:119], v[148:149], v[136:137] op_sel_hi:[0,1]
	v_pk_mul_f32 v[122:123], v[148:149], v[136:137] op_sel:[1,0]
	v_pk_fma_f32 v[94:95], v[148:149], v[140:141], v[94:95] op_sel_hi:[0,1,1]
	v_pk_fma_f32 v[118:119], v[150:151], v[140:141], v[118:119] op_sel_hi:[0,1,1]
	v_pk_fma_f32 v[122:123], v[150:151], v[140:141], v[122:123] op_sel:[1,0,0]
	v_pk_fma_f32 v[94:95], v[148:149], v[152:153], v[94:95] op_sel:[1,0,0]
	v_pk_fma_f32 v[118:119], v[150:151], v[152:153], v[118:119] op_sel:[1,0,0]
	v_pk_fma_f32 v[122:123], v[156:157], v[152:153], v[122:123] op_sel_hi:[0,1,1]
	v_pk_mul_f32 v[160:161], v[144:145], v[94:95] op_sel_hi:[0,1]
	v_pk_fma_f32 v[160:161], v[144:145], v[118:119], v[160:161] op_sel:[1,0,0]
	v_pk_fma_f32 v[160:161], v[146:147], v[122:123], v[160:161] op_sel_hi:[0,1,1]
	v_pk_fma_f32 v[160:161], v[156:157], v[70:71], v[160:161] op_sel:[1,0,0] neg_lo:[0,0,1] neg_hi:[0,0,1]
	v_cmp_eq_u32_e64 s[10:11], 6, v159
	v_cmp_eq_u32_e64 s[14:15], 7, v159
	v_pk_add_f32 v[70:71], v[138:139], v[94:95]
	v_pk_add_f32 v[130:131], v[46:47], v[118:119]
	v_pk_add_f32 v[46:47], v[50:51], v[122:123]
	v_pk_add_f32 v[136:137], v[112:113], v[160:161]
	v_pk_fma_f32 v[112:113], v[100:101], v[70:71], v[136:137] op_sel_hi:[0,1,1]
	v_pk_fma_f32 v[140:141], v[108:109], v[70:71], v[136:137] op_sel_hi:[0,1,1]
	v_pk_fma_f32 v[112:113], v[100:101], v[130:131], v[112:113] op_sel:[1,0,0]
	v_pk_fma_f32 v[140:141], v[108:109], v[130:131], v[140:141] op_sel:[1,0,0]
	v_pk_fma_f32 v[112:113], v[102:103], v[46:47], v[112:113] op_sel_hi:[0,1,1]
	v_pk_fma_f32 v[140:141], v[110:111], v[46:47], v[140:141] op_sel_hi:[0,1,1]
	v_pk_fma_f32 v[136:137], v[8:9], v[70:71], v[136:137] op_sel_hi:[0,1,1]
	v_pk_fma_f32 v[136:137], v[8:9], v[130:131], v[136:137] op_sel:[1,0,0]
	v_pk_fma_f32 v[136:137], v[10:11], v[46:47], v[136:137] op_sel_hi:[0,1,1]
	v_cndmask_b32_e64 v50, 0, v18, s[10:11]
	v_cndmask_b32_e64 v51, 0, v18, s[14:15]
	v_add_f32_dpp v136, v112, v136 wave_shl:1 row_mask:0xf bank_mask:0xf bound_ctrl:1
	v_add_f32_dpp v137, v113, v137 wave_shl:1 row_mask:0xf bank_mask:0xf bound_ctrl:1
	s_add_i32 s4, s34, 3
	s_cmpk_lt_i32 s4, 0x201
	s_cselect_b64 s[12:13], s[0:1], 0
	v_add_f32_dpp v136, v140, v136 wave_shr:1 row_mask:0xf bank_mask:0xf bound_ctrl:1
	v_add_f32_dpp v137, v141, v137 wave_shr:1 row_mask:0xf bank_mask:0xf bound_ctrl:1
	v_pk_fma_f32 v[136:137], v[4:5], v[158:159], v[136:137] op_sel_hi:[1,0,1] neg_lo:[0,0,1] neg_hi:[0,0,1]
	v_pk_add_f32 v[136:137], v[136:137], v[50:51] neg_lo:[0,1] neg_hi:[0,1]
	v_pk_mul_f32 v[134:135], v[136:137], v[136:137]
	v_add_f32_e32 v134, v134, v135
	v_cndmask_b32_e64 v135, 0, v134, s[12:13]
	v_add_f32_e32 v1, v1, v135
	s_add_i32 s5, s34, 8
	s_min_i32 s5, s5, 0x200
	s_mul_i32 s6, s5, 0x804
	s_add_i32 s6, s6, s35
	s_add_i32 s7, s6, 0x505014
	s_add_i32 s8, s6, 0x606018
	s_mul_i32 s9, s5, 0x180c
	s_add_i32 s9, s9, s33
	s_add_i32 s4, s34, 9
	s_min_i32 s4, s4, 0x200
	s_mul_i32 s4, s4, 0x804
	s_add_i32 s4, s4, s38
	buffer_load_dword v17, v28, s[20:23], s4 offen nt
	buffer_load_dwordx3 v[8:10], v27, s[24:27], s9 offen nt
	buffer_load_dword v4, v28, s[16:19], s7 offen nt
	buffer_load_dword v5, v28, s[16:19], s8 offen nt
	s_waitcnt vmcnt(8)
	v_mov_b32_dpp v100, v40 wave_shr:1 row_mask:0xf bank_mask:0xf bound_ctrl:1
	v_mov_b32_dpp v101, v41 wave_shr:1 row_mask:0xf bank_mask:0xf bound_ctrl:1
	v_mov_b32_dpp v102, v42 wave_shr:1 row_mask:0xf bank_mask:0xf bound_ctrl:1
	v_mov_b32_dpp v108, v40 wave_shl:1 row_mask:0xf bank_mask:0xf bound_ctrl:1
	v_mov_b32_dpp v109, v41 wave_shl:1 row_mask:0xf bank_mask:0xf bound_ctrl:1
	v_mov_b32_dpp v110, v42 wave_shl:1 row_mask:0xf bank_mask:0xf bound_ctrl:1
	s_add_i32 s4, s34, 7
	s_cmpk_lt_u32 s4, 0x201
	s_cselect_b64 s[12:13], s[40:41], 0
	v_cmp_eq_u32_e64 s[14:15], s37, v25
	s_and_b64 s[14:15], s[14:15], s[12:13]
	v_cndmask_b32_e64 v29, 0, 1, s[14:15]
	v_pk_add_f32 v[46:47], v[40:41], v[100:101]
	v_pk_mul_f32 v[50:51], v[40:41], v[40:41] op_sel_hi:[0,1]
	v_or_b32_dpp v31, v29, v29 wave_shr:1 row_mask:0xf bank_mask:0xf bound_ctrl:1
	v_pk_mul_f32 v[70:71], v[40:41], v[42:43] op_sel_hi:[1,0]
	v_or_b32_dpp v31, v29, v31 wave_shl:1 row_mask:0xf bank_mask:0xf bound_ctrl:1
	v_mul_f32_e64 v112, v41, v41
	v_mul_f32_e64 v113, v42, v42
	v_or_b32_dpp v57, v31, v31 wave_shr:1 row_mask:0xf bank_mask:0xf bound_ctrl:1
	v_add_f32_e64 v130, v42, v102
	v_pk_add_f32 v[46:47], v[46:47], v[108:109]
	v_or_b32_dpp v57, v31, v57 wave_shl:1 row_mask:0xf bank_mask:0xf bound_ctrl:1
	v_or3_b32 v29, v57, v88, v89
	v_or3_b32 v29, v29, v56, v30
	s_add_i32 s4, s34, 4
	s_cmpk_lt_u32 s4, 0x1ff
	s_cselect_b64 s[12:13], s[42:43], 0
	v_cmp_ne_u32_e64 s[30:31], 0, v29
	s_and_b64 s[30:31], s[30:31], s[12:13]
	v_cndmask_b32_e64 v29, 0, 1.0, s[30:31]
	v_pk_fma_f32 v[50:51], v[100:101], v[100:101], v[50:51] op_sel_hi:[0,1,1]
	v_pk_fma_f32 v[70:71], v[100:101], v[102:103], v[70:71] op_sel_hi:[1,0,1]
	v_fma_f32 v112, v101, v101, v112
	v_fma_f32 v113, v102, v102, v113
	v_add_f32_dpp v131, v29, v29 wave_shr:1 row_mask:0xf bank_mask:0xf bound_ctrl:1
	v_add_f32_e64 v130, v130, v110
	v_pk_fma_f32 v[50:51], v[108:109], v[108:109], v[50:51] op_sel_hi:[0,1,1]
	v_pk_fma_f32 v[70:71], v[108:109], v[110:111], v[70:71] op_sel_hi:[1,0,1]
	v_fma_f32 v112, v109, v109, v112
	v_fma_f32 v113, v110, v110, v113
	v_add_f32_dpp v131, v29, v131 wave_shl:1 row_mask:0xf bank_mask:0xf bound_ctrl:1
	v_pk_add_f32 v[136:137], v[64:65], v[46:47]
	v_pk_add_f32 v[134:135], v[38:39], v[136:137]
	v_pk_add_f32 v[38:39], v[84:85], v[50:51]
	v_pk_add_f32 v[64:65], v[52:53], v[38:39]
	v_pk_add_f32 v[52:53], v[92:93], v[70:71]
	v_pk_add_f32 v[84:85], v[58:59], v[52:53]
	v_pk_add_f32 v[92:93], v[96:97], v[112:113]
	v_pk_add_f32 v[58:59], v[98:99], v[92:93]
	v_pk_add_f32 v[96:97], v[116:117], v[130:131]
	v_pk_add_f32 v[98:99], v[114:115], v[96:97]
	v_mul_f32_e64 v140, v134, v22
	v_mul_f32_e64 v141, v135, v22
	v_mul_f32_e64 v142, v98, v22
	v_fma_f32 v29, v64, v22, v26
	v_mul_f32_e64 v31, v65, v22
	v_mul_f32_e64 v114, v84, v22
	v_fma_f32 v115, v58, v22, v26
	v_mul_f32_e64 v116, v85, v22
	v_fma_f32 v117, v59, v22, v26
	v_fma_f32 v29, -v140, v140, v29
	v_fma_f32 v31, -v140, v141, v31
	v_fma_f32 v114, -v140, v142, v114
	v_fma_f32 v115, -v141, v141, v115
	v_fma_f32 v116, -v141, v142, v116
	v_fma_f32 v117, -v142, v142, v117
	v_mul_f32_e64 v138, v116, v116
	v_mul_f32_e64 v139, v31, v117
	v_mul_f32_e64 v152, v114, v115
	v_mul_f32_e64 v153, v114, v114
	v_mul_f32_e64 v154, v29, v116
	v_mul_f32_e64 v155, v31, v31
	v_fma_f32 v138, v115, v117, -v138
	v_fma_f32 v139, v114, v116, -v139
	v_fma_f32 v152, v31, v116, -v152
	v_fma_f32 v153, v29, v117, -v153
	v_fma_f32 v154, v31, v114, -v154
	v_fma_f32 v155, v29, v115, -v155
	v_mul_f32_e64 v156, v29, v138
	v_fma_f32 v156, v31, v139, v156
	v_fma_f32 v156, v114, v152, v156
	v_rcp_f32_e32 v156, v156
	v_cmp_ne_u32_e64 vcc, s37, v2
	v_mul_f32_e64 v156, v156, v22
	v_cndmask_b32_e64 v156, 0, v156, s[30:31]
	v_cndmask_b32_e64 v29, 0, v18, vcc
	v_cndmask_b32_e64 v149, 0, v22, s[30:31]
	v_mul_f32_e64 v143, v138, v156
	v_mul_f32_e64 v144, v139, v156
	v_mul_f32_e64 v145, v152, v156
	v_mul_f32_e64 v146, v153, v156
	v_mul_f32_e64 v147, v154, v156
	v_mul_f32_e64 v148, v155, v156
	v_add_f32_e64 v150, v99, v29
	v_mov_b32_e32 v151, v2
	ds_write_b128 v23, v[140:143]
	ds_write_b128 v23, v[144:147] offset:1024
	ds_write_b128 v23, v[148:151] offset:2048
	v_mov_b32_dpp v30, v36 wave_shr:1 row_mask:0xf bank_mask:0xf bound_ctrl:1
	v_mov_b32_dpp v31, v37 wave_shr:1 row_mask:0xf bank_mask:0xf bound_ctrl:1
	v_mov_b32_dpp v58, v36 wave_shl:1 row_mask:0xf bank_mask:0xf bound_ctrl:1
	v_mov_b32_dpp v59, v37 wave_shl:1 row_mask:0xf bank_mask:0xf bound_ctrl:1
	v_pk_mul_f32 v[64:65], v[36:37], v[40:41] op_sel_hi:[1,0]
	v_pk_mul_f32 v[84:85], v[36:37], v[40:41] op_sel:[0,1]
	v_pk_mul_f32 v[116:117], v[36:37], v[42:43] op_sel_hi:[1,0]
	v_pk_add_f32 v[152:153], v[36:37], v[30:31]
	v_pk_fma_f32 v[64:65], v[30:31], v[100:101], v[64:65] op_sel_hi:[1,0,1]
	v_pk_fma_f32 v[84:85], v[30:31], v[100:101], v[84:85] op_sel:[0,1,0]
	v_pk_fma_f32 v[116:117], v[30:31], v[102:103], v[116:117] op_sel_hi:[1,0,1]
	v_pk_add_f32 v[152:153], v[152:153], v[58:59]
	v_pk_fma_f32 v[64:65], v[58:59], v[108:109], v[64:65] op_sel_hi:[1,0,1]
	v_pk_fma_f32 v[84:85], v[58:59], v[108:109], v[84:85] op_sel:[0,1,0]
	v_pk_fma_f32 v[116:117], v[58:59], v[110:111], v[116:117] op_sel_hi:[1,0,1]
	s_waitcnt lgkmcnt(0)
	s_barrier
	v_pk_add_f32 v[156:157], v[132:133], v[152:153]
	v_pk_add_f32 v[30:31], v[90:91], v[156:157]
	v_pk_add_f32 v[132:133], v[48:49], v[64:65]
	v_pk_add_f32 v[164:165], v[54:55], v[132:133]
	v_pk_add_f32 v[48:49], v[120:121], v[84:85]
	v_pk_add_f32 v[168:169], v[66:67], v[48:49]
	v_pk_add_f32 v[120:121], v[128:129], v[116:117]
	v_pk_add_f32 v[172:173], v[86:87], v[120:121]
	v_pk_fma_f32 v[164:165], v[140:141], v[30:31], v[164:165] op_sel_hi:[0,1,1] neg_lo:[1,0,0] neg_hi:[1,0,0]
	v_pk_fma_f32 v[168:169], v[140:141], v[30:31], v[168:169] op_sel:[1,0,0] neg_lo:[1,0,0] neg_hi:[1,0,0]
	v_pk_fma_f32 v[172:173], v[142:143], v[30:31], v[172:173] op_sel_hi:[0,1,1] neg_lo:[1,0,0] neg_hi:[1,0,0]
	v_pk_mul_f32 v[54:55], v[142:143], v[164:165] op_sel:[1,0]
	v_pk_mul_f32 v[58:59], v[144:145], v[164:165] op_sel_hi:[0,1]
	v_pk_mul_f32 v[66:67], v[144:145], v[164:165] op_sel:[1,0]
	v_pk_fma_f32 v[54:55], v[144:145], v[168:169], v[54:55] op_sel_hi:[0,1,1]
	v_pk_fma_f32 v[58:59], v[146:147], v[168:169], v[58:59] op_sel_hi:[0,1,1]
	v_pk_fma_f32 v[66:67], v[146:147], v[168:169], v[66:67] op_sel:[1,0,0]
	v_pk_fma_f32 v[54:55], v[144:145], v[172:173], v[54:55] op_sel:[1,0,0]
	v_pk_fma_f32 v[58:59], v[146:147], v[172:173], v[58:59] op_sel:[1,0,0]
	v_pk_fma_f32 v[66:67], v[148:149], v[172:173], v[66:67] op_sel_hi:[0,1,1]
	v_pk_mul_f32 v[128:129], v[140:141], v[54:55] op_sel_hi:[0,1]
	v_pk_fma_f32 v[128:129], v[140:141], v[58:59], v[128:129] op_sel:[1,0,0]
	v_pk_fma_f32 v[128:129], v[142:143], v[66:67], v[128:129] op_sel_hi:[0,1,1]
	v_pk_fma_f32 v[128:129], v[148:149], v[30:31], v[128:129] op_sel:[1,0,0] neg_lo:[0,0,1] neg_hi:[0,0,1]
	v_cmp_eq_u32_e64 s[10:11], 6, v151
	v_cmp_eq_u32_e64 s[14:15], 7, v151
	v_pk_add_f32 v[30:31], v[94:95], v[54:55]
	v_pk_add_f32 v[86:87], v[44:45], v[30:31]
	v_pk_add_f32 v[90:91], v[118:119], v[58:59]
	v_pk_add_f32 v[44:45], v[60:61], v[90:91]
	v_pk_add_f32 v[94:95], v[122:123], v[66:67]
	v_pk_add_f32 v[60:61], v[68:69], v[94:95]
	v_pk_add_f32 v[68:69], v[160:161], v[128:129]
	v_pk_add_f32 v[98:99], v[162:163], v[68:69]
	v_pk_fma_f32 v[114:115], v[72:73], v[86:87], v[98:99] op_sel_hi:[0,1,1]
	v_pk_fma_f32 v[118:119], v[124:125], v[86:87], v[98:99] op_sel_hi:[0,1,1]
	v_pk_fma_f32 v[114:115], v[72:73], v[44:45], v[114:115] op_sel:[1,0,0]
	v_pk_fma_f32 v[118:119], v[124:125], v[44:45], v[118:119] op_sel:[1,0,0]
	v_pk_fma_f32 v[114:115], v[74:75], v[60:61], v[114:115] op_sel_hi:[0,1,1]
	v_pk_fma_f32 v[118:119], v[126:127], v[60:61], v[118:119] op_sel_hi:[0,1,1]
	v_pk_fma_f32 v[98:99], v[12:13], v[86:87], v[98:99] op_sel_hi:[0,1,1]
	v_pk_fma_f32 v[98:99], v[12:13], v[44:45], v[98:99] op_sel:[1,0,0]
	v_pk_fma_f32 v[98:99], v[14:15], v[60:61], v[98:99] op_sel_hi:[0,1,1]
	v_cndmask_b32_e64 v160, 0, v18, s[10:11]
	v_cndmask_b32_e64 v161, 0, v18, s[14:15]
	v_add_f32_dpp v98, v114, v98 wave_shl:1 row_mask:0xf bank_mask:0xf bound_ctrl:1
	v_add_f32_dpp v99, v115, v99 wave_shl:1 row_mask:0xf bank_mask:0xf bound_ctrl:1
	s_add_i32 s4, s34, 4
	s_cmpk_lt_i32 s4, 0x201
	s_cselect_b64 s[12:13], s[0:1], 0
	v_add_f32_dpp v98, v118, v98 wave_shr:1 row_mask:0xf bank_mask:0xf bound_ctrl:1
	v_add_f32_dpp v99, v119, v99 wave_shr:1 row_mask:0xf bank_mask:0xf bound_ctrl:1
	v_pk_fma_f32 v[98:99], v[6:7], v[150:151], v[98:99] op_sel_hi:[1,0,1] neg_lo:[0,0,1] neg_hi:[0,0,1]
	v_pk_add_f32 v[98:99], v[98:99], v[160:161] neg_lo:[0,1] neg_hi:[0,1]
	v_pk_mul_f32 v[122:123], v[98:99], v[98:99]
	v_add_f32_e32 v122, v122, v123
	v_cndmask_b32_e64 v123, 0, v122, s[12:13]
	v_add_f32_e32 v1, v1, v123
	s_add_i32 s5, s34, 9
	s_min_i32 s5, s5, 0x200
	s_mul_i32 s6, s5, 0x804
	s_add_i32 s6, s6, s35
	s_add_i32 s7, s6, 0x505014
	s_add_i32 s8, s6, 0x606018
	s_mul_i32 s9, s5, 0x180c
	s_add_i32 s9, s9, s33
	s_add_i32 s4, s34, 10
	s_min_i32 s4, s4, 0x200
	s_mul_i32 s4, s4, 0x804
	s_add_i32 s4, s4, s38
	buffer_load_dword v2, v28, s[20:23], s4 offen nt
	buffer_load_dwordx3 v[12:14], v27, s[24:27], s9 offen nt
	buffer_load_dword v6, v28, s[16:19], s7 offen nt
	buffer_load_dword v7, v28, s[16:19], s8 offen nt
	s_waitcnt vmcnt(8)
	v_mov_b32_dpp v72, v76 wave_shr:1 row_mask:0xf bank_mask:0xf bound_ctrl:1
	v_mov_b32_dpp v73, v77 wave_shr:1 row_mask:0xf bank_mask:0xf bound_ctrl:1
	v_mov_b32_dpp v74, v78 wave_shr:1 row_mask:0xf bank_mask:0xf bound_ctrl:1
	v_mov_b32_dpp v124, v76 wave_shl:1 row_mask:0xf bank_mask:0xf bound_ctrl:1
	v_mov_b32_dpp v125, v77 wave_shl:1 row_mask:0xf bank_mask:0xf bound_ctrl:1
	v_mov_b32_dpp v126, v78 wave_shl:1 row_mask:0xf bank_mask:0xf bound_ctrl:1
	s_add_i32 s4, s34, 8
	s_cmpk_lt_u32 s4, 0x201
	s_cselect_b64 s[12:13], s[40:41], 0
	v_cmp_eq_u32_e64 s[14:15], s37, v24
	s_and_b64 s[14:15], s[14:15], s[12:13]
	v_cndmask_b32_e64 v29, 0, 1, s[14:15]
	v_pk_add_f32 v[44:45], v[76:77], v[72:73]
	v_pk_mul_f32 v[60:61], v[76:77], v[76:77] op_sel_hi:[0,1]
	v_or_b32_dpp v118, v29, v29 wave_shr:1 row_mask:0xf bank_mask:0xf bound_ctrl:1
	v_pk_mul_f32 v[86:87], v[76:77], v[78:79] op_sel_hi:[1,0]
	v_or_b32_dpp v118, v29, v118 wave_shl:1 row_mask:0xf bank_mask:0xf bound_ctrl:1
	v_mul_f32_e64 v98, v77, v77
	v_mul_f32_e64 v99, v78, v78
	v_or_b32_dpp v119, v118, v118 wave_shr:1 row_mask:0xf bank_mask:0xf bound_ctrl:1
	v_add_f32_e64 v114, v78, v74
	v_pk_add_f32 v[44:45], v[44:45], v[124:125]
	v_or_b32_dpp v119, v118, v119 wave_shl:1 row_mask:0xf bank_mask:0xf bound_ctrl:1
	v_or3_b32 v29, v119, v57, v88
	v_or3_b32 v29, v29, v89, v56
	s_add_i32 s4, s34, 5
	s_cmpk_lt_u32 s4, 0x1ff
	s_cselect_b64 s[12:13], s[42:43], 0
	v_cmp_ne_u32_e64 s[30:31], 0, v29
	s_and_b64 s[30:31], s[30:31], s[12:13]
	v_cndmask_b32_e64 v29, 0, 1.0, s[30:31]
	v_pk_fma_f32 v[60:61], v[72:73], v[72:73], v[60:61] op_sel_hi:[0,1,1]
	v_pk_fma_f32 v[86:87], v[72:73], v[74:75], v[86:87] op_sel_hi:[1,0,1]
	v_fma_f32 v98, v73, v73, v98
	v_fma_f32 v99, v74, v74, v99
	v_add_f32_dpp v115, v29, v29 wave_shr:1 row_mask:0xf bank_mask:0xf bound_ctrl:1
	v_add_f32_e64 v114, v114, v126
	v_pk_fma_f32 v[60:61], v[124:125], v[124:125], v[60:61] op_sel_hi:[0,1,1]
	v_pk_fma_f32 v[86:87], v[124:125], v[126:127], v[86:87] op_sel_hi:[1,0,1]
	v_fma_f32 v98, v125, v125, v98
	v_fma_f32 v99, v126, v126, v99
	v_add_f32_dpp v115, v29, v115 wave_shl:1 row_mask:0xf bank_mask:0xf bound_ctrl:1
	v_pk_add_f32 v[122:123], v[136:137], v[44:45]
	v_pk_add_f32 v[134:135], v[38:39], v[60:61]
	v_pk_add_f32 v[38:39], v[52:53], v[86:87]
	v_pk_add_f32 v[52:53], v[92:93], v[98:99]
	v_pk_add_f32 v[92:93], v[96:97], v[114:115]
	v_mul_f32_e64 v136, v122, v22
	v_mul_f32_e64 v137, v123, v22
	v_mul_f32_e64 v138, v92, v22
	v_fma_f32 v29, v134, v22, v26
	v_mul_f32_e64 v118, v135, v22
	v_mul_f32_e64 v96, v38, v22
	v_fma_f32 v97, v52, v22, v26
	v_mul_f32_e64 v148, v39, v22
	v_fma_f32 v149, v53, v22, v26
	v_fma_f32 v29, -v136, v136, v29
	v_fma_f32 v118, -v136, v137, v118
	v_fma_f32 v96, -v136, v138, v96
	v_fma_f32 v97, -v137, v137, v97
	v_fma_f32 v148, -v137, v138, v148
	v_fma_f32 v149, -v138, v138, v149
	v_mul_f32_e64 v150, v148, v148
	v_mul_f32_e64 v151, v118, v149
	v_mul_f32_e64 v154, v96, v97
	v_mul_f32_e64 v155, v96, v96
	v_mul_f32_e64 v158, v29, v148
	v_mul_f32_e64 v159, v118, v118
	v_fma_f32 v150, v97, v149, -v150
	v_fma_f32 v151, v96, v148, -v151
	v_fma_f32 v154, v118, v148, -v154
	v_fma_f32 v155, v29, v149, -v155
	v_fma_f32 v158, v118, v96, -v158
	v_fma_f32 v159, v29, v97, -v159
	v_mul_f32_e64 v160, v29, v150
	v_fma_f32 v160, v118, v151, v160
	v_fma_f32 v160, v96, v154, v160
	v_rcp_f32_e32 v160, v160
	v_cmp_ne_u32_e64 vcc, s37, v3
	v_mul_f32_e64 v160, v160, v22
	v_cndmask_b32_e64 v160, 0, v160, s[30:31]
	v_cndmask_b32_e64 v29, 0, v18, vcc
	v_cndmask_b32_e64 v145, 0, v22, s[30:31]
	v_mul_f32_e64 v139, v150, v160
	v_mul_f32_e64 v140, v151, v160
	v_mul_f32_e64 v141, v154, v160
	v_mul_f32_e64 v142, v155, v160
	v_mul_f32_e64 v143, v158, v160
	v_mul_f32_e64 v144, v159, v160
	v_add_f32_e64 v146, v93, v29
	v_mov_b32_e32 v147, v3
	ds_write_b128 v23, v[136:139] offset:3072
	ds_write_b128 v23, v[140:143] offset:4096
	ds_write_b128 v23, v[144:147] offset:5120
	v_mov_b32_dpp v52, v62 wave_shr:1 row_mask:0xf bank_mask:0xf bound_ctrl:1
	v_mov_b32_dpp v53, v63 wave_shr:1 row_mask:0xf bank_mask:0xf bound_ctrl:1
	v_mov_b32_dpp v92, v62 wave_shl:1 row_mask:0xf bank_mask:0xf bound_ctrl:1
	v_mov_b32_dpp v93, v63 wave_shl:1 row_mask:0xf bank_mask:0xf bound_ctrl:1
	v_pk_mul_f32 v[38:39], v[62:63], v[76:77] op_sel_hi:[1,0]
	v_pk_mul_f32 v[122:123], v[62:63], v[76:77] op_sel:[0,1]
	v_pk_mul_f32 v[134:135], v[62:63], v[78:79] op_sel_hi:[1,0]
	v_pk_add_f32 v[150:151], v[62:63], v[52:53]
	v_pk_fma_f32 v[38:39], v[52:53], v[72:73], v[38:39] op_sel_hi:[1,0,1]
	v_pk_fma_f32 v[122:123], v[52:53], v[72:73], v[122:123] op_sel:[0,1,0]
	v_pk_fma_f32 v[134:135], v[52:53], v[74:75], v[134:135] op_sel_hi:[1,0,1]
	v_pk_add_f32 v[150:151], v[150:151], v[92:93]
	v_pk_fma_f32 v[38:39], v[92:93], v[124:125], v[38:39] op_sel_hi:[1,0,1]
	v_pk_fma_f32 v[122:123], v[92:93], v[124:125], v[122:123] op_sel:[0,1,0]
	v_pk_fma_f32 v[134:135], v[92:93], v[126:127], v[134:135] op_sel_hi:[1,0,1]
	s_waitcnt lgkmcnt(0)
	s_barrier
	v_pk_add_f32 v[52:53], v[156:157], v[150:151]
	v_pk_add_f32 v[154:155], v[132:133], v[38:39]
	v_pk_add_f32 v[158:159], v[48:49], v[122:123]
	v_pk_add_f32 v[162:163], v[120:121], v[134:135]
	v_pk_fma_f32 v[154:155], v[136:137], v[52:53], v[154:155] op_sel_hi:[0,1,1] neg_lo:[1,0,0] neg_hi:[1,0,0]
	v_pk_fma_f32 v[158:159], v[136:137], v[52:53], v[158:159] op_sel:[1,0,0] neg_lo:[1,0,0] neg_hi:[1,0,0]
	v_pk_fma_f32 v[162:163], v[138:139], v[52:53], v[162:163] op_sel_hi:[0,1,1] neg_lo:[1,0,0] neg_hi:[1,0,0]
	v_pk_mul_f32 v[48:49], v[138:139], v[154:155] op_sel:[1,0]
	v_pk_mul_f32 v[92:93], v[140:141], v[154:155] op_sel_hi:[0,1]
	v_pk_mul_f32 v[96:97], v[140:141], v[154:155] op_sel:[1,0]
	v_pk_fma_f32 v[48:49], v[140:141], v[158:159], v[48:49] op_sel_hi:[0,1,1]
	v_pk_fma_f32 v[92:93], v[142:143], v[158:159], v[92:93] op_sel_hi:[0,1,1]
	v_pk_fma_f32 v[96:97], v[142:143], v[158:159], v[96:97] op_sel:[1,0,0]
	v_pk_fma_f32 v[48:49], v[140:141], v[162:163], v[48:49] op_sel:[1,0,0]
	v_pk_fma_f32 v[92:93], v[142:143], v[162:163], v[92:93] op_sel:[1,0,0]
	v_pk_fma_f32 v[96:97], v[144:145], v[162:163], v[96:97] op_sel_hi:[0,1,1]
	v_pk_mul_f32 v[166:167], v[136:137], v[48:49] op_sel_hi:[0,1]
	v_pk_fma_f32 v[166:167], v[136:137], v[92:93], v[166:167] op_sel:[1,0,0]
	v_pk_fma_f32 v[166:167], v[138:139], v[96:97], v[166:167] op_sel_hi:[0,1,1]
	v_pk_fma_f32 v[166:167], v[144:145], v[52:53], v[166:167] op_sel:[1,0,0] neg_lo:[0,0,1] neg_hi:[0,0,1]
	v_cmp_eq_u32_e64 s[10:11], 6, v147
	v_cmp_eq_u32_e64 s[14:15], 7, v147
	v_pk_add_f32 v[52:53], v[30:31], v[48:49]
	v_pk_add_f32 v[30:31], v[90:91], v[92:93]
	v_pk_add_f32 v[90:91], v[94:95], v[96:97]
	v_pk_add_f32 v[120:121], v[68:69], v[166:167]
	v_pk_fma_f32 v[68:69], v[80:81], v[52:53], v[120:121] op_sel_hi:[0,1,1]
	v_pk_fma_f32 v[132:133], v[104:105], v[52:53], v[120:121] op_sel_hi:[0,1,1]
	v_pk_fma_f32 v[68:69], v[80:81], v[30:31], v[68:69] op_sel:[1,0,0]
	v_pk_fma_f32 v[132:133], v[104:105], v[30:31], v[132:133] op_sel:[1,0,0]
	v_pk_fma_f32 v[68:69], v[82:83], v[90:91], v[68:69] op_sel_hi:[0,1,1]
	v_pk_fma_f32 v[132:133], v[106:107], v[90:91], v[132:133] op_sel_hi:[0,1,1]
	v_pk_fma_f32 v[120:121], v[32:33], v[52:53], v[120:121] op_sel_hi:[0,1,1]
	v_pk_fma_f32 v[120:121], v[32:33], v[30:31], v[120:121] op_sel:[1,0,0]
	v_pk_fma_f32 v[120:121], v[34:35], v[90:91], v[120:121] op_sel_hi:[0,1,1]
	v_cndmask_b32_e64 v94, 0, v18, s[10:11]
	v_cndmask_b32_e64 v95, 0, v18, s[14:15]
	v_add_f32_dpp v120, v68, v120 wave_shl:1 row_mask:0xf bank_mask:0xf bound_ctrl:1
	v_add_f32_dpp v121, v69, v121 wave_shl:1 row_mask:0xf bank_mask:0xf bound_ctrl:1
	s_add_i32 s4, s34, 5
	s_cmpk_lt_i32 s4, 0x201
	s_cselect_b64 s[12:13], s[0:1], 0
	v_add_f32_dpp v120, v132, v120 wave_shr:1 row_mask:0xf bank_mask:0xf bound_ctrl:1
	v_add_f32_dpp v121, v133, v121 wave_shr:1 row_mask:0xf bank_mask:0xf bound_ctrl:1
	v_pk_fma_f32 v[120:121], v[20:21], v[146:147], v[120:121] op_sel_hi:[1,0,1] neg_lo:[0,0,1] neg_hi:[0,0,1]
	v_pk_add_f32 v[120:121], v[120:121], v[94:95] neg_lo:[0,1] neg_hi:[0,1]
	v_pk_mul_f32 v[148:149], v[120:121], v[120:121]
	v_add_f32_e32 v148, v148, v149
	v_cndmask_b32_e64 v149, 0, v148, s[12:13]
	v_add_f32_e32 v1, v1, v149
	s_add_i32 s5, s34, 10
	s_min_i32 s5, s5, 0x200
	s_mul_i32 s6, s5, 0x804
	s_add_i32 s6, s6, s35
	s_add_i32 s7, s6, 0x505014
	s_add_i32 s8, s6, 0x606018
	s_mul_i32 s9, s5, 0x180c
	s_add_i32 s9, s9, s33
	s_add_i32 s4, s34, 11
	s_min_i32 s4, s4, 0x200
	s_mul_i32 s4, s4, 0x804
	s_add_i32 s4, s4, s38
	buffer_load_dword v3, v28, s[20:23], s4 offen nt
	buffer_load_dwordx3 v[32:34], v27, s[24:27], s9 offen nt
	buffer_load_dword v20, v28, s[16:19], s7 offen nt
	buffer_load_dword v21, v28, s[16:19], s8 offen nt
	s_waitcnt vmcnt(8)
	v_mov_b32_dpp v80, v8 wave_shr:1 row_mask:0xf bank_mask:0xf bound_ctrl:1
	v_mov_b32_dpp v81, v9 wave_shr:1 row_mask:0xf bank_mask:0xf bound_ctrl:1
	v_mov_b32_dpp v82, v10 wave_shr:1 row_mask:0xf bank_mask:0xf bound_ctrl:1
	v_mov_b32_dpp v104, v8 wave_shl:1 row_mask:0xf bank_mask:0xf bound_ctrl:1
	v_mov_b32_dpp v105, v9 wave_shl:1 row_mask:0xf bank_mask:0xf bound_ctrl:1
	v_mov_b32_dpp v106, v10 wave_shl:1 row_mask:0xf bank_mask:0xf bound_ctrl:1
	s_add_i32 s4, s34, 9
	s_cmpk_lt_u32 s4, 0x201
	s_cselect_b64 s[12:13], s[40:41], 0
	v_cmp_eq_u32_e64 s[14:15], s37, v17
	s_and_b64 s[14:15], s[14:15], s[12:13]
	v_cndmask_b32_e64 v29, 0, 1, s[14:15]
	v_pk_add_f32 v[30:31], v[8:9], v[80:81]
	v_pk_mul_f32 v[52:53], v[8:9], v[8:9] op_sel_hi:[0,1]
	v_or_b32_dpp v56, v29, v29 wave_shr:1 row_mask:0xf bank_mask:0xf bound_ctrl:1
	v_pk_mul_f32 v[68:69], v[8:9], v[10:11] op_sel_hi:[1,0]
	v_or_b32_dpp v56, v29, v56 wave_shl:1 row_mask:0xf bank_mask:0xf bound_ctrl:1
	v_mul_f32_e64 v90, v9, v9
	v_mul_f32_e64 v91, v10, v10
	v_or_b32_dpp v118, v56, v56 wave_shr:1 row_mask:0xf bank_mask:0xf bound_ctrl:1
	v_add_f32_e64 v94, v10, v82
	v_pk_add_f32 v[30:31], v[30:31], v[104:105]
	v_or_b32_dpp v118, v56, v118 wave_shl:1 row_mask:0xf bank_mask:0xf bound_ctrl:1
	v_or3_b32 v29, v118, v119, v57
	v_or3_b32 v29, v29, v88, v89
	s_add_i32 s4, s34, 6
	s_cmpk_lt_u32 s4, 0x1ff
	s_cselect_b64 s[12:13], s[42:43], 0
	v_cmp_ne_u32_e64 s[30:31], 0, v29
	s_and_b64 s[30:31], s[30:31], s[12:13]
	v_cndmask_b32_e64 v29, 0, 1.0, s[30:31]
	v_pk_fma_f32 v[52:53], v[80:81], v[80:81], v[52:53] op_sel_hi:[0,1,1]
	v_pk_fma_f32 v[68:69], v[80:81], v[82:83], v[68:69] op_sel_hi:[1,0,1]
	v_fma_f32 v90, v81, v81, v90
	v_fma_f32 v91, v82, v82, v91
	v_add_f32_dpp v95, v29, v29 wave_shr:1 row_mask:0xf bank_mask:0xf bound_ctrl:1
	v_add_f32_e64 v94, v94, v106
	v_pk_fma_f32 v[52:53], v[104:105], v[104:105], v[52:53] op_sel_hi:[0,1,1]
	v_pk_fma_f32 v[68:69], v[104:105], v[106:107], v[68:69] op_sel_hi:[1,0,1]
	v_fma_f32 v90, v105, v105, v90
	v_fma_f32 v91, v106, v106, v91
	v_add_f32_dpp v95, v29, v95 wave_shl:1 row_mask:0xf bank_mask:0xf bound_ctrl:1
	v_pk_add_f32 v[120:121], v[44:45], v[30:31]
	v_pk_add_f32 v[132:133], v[46:47], v[120:121]
	v_pk_add_f32 v[44:45], v[60:61], v[52:53]
	v_pk_add_f32 v[46:47], v[50:51], v[44:45]
	v_pk_add_f32 v[60:61], v[86:87], v[68:69]
	v_pk_add_f32 v[50:51], v[70:71], v[60:61]
	v_pk_add_f32 v[70:71], v[98:99], v[90:91]
	v_pk_add_f32 v[86:87], v[112:113], v[70:71]
	v_pk_add_f32 v[112:113], v[114:115], v[94:95]
	v_pk_add_f32 v[98:99], v[130:131], v[112:113]
	v_mul_f32_e64 v136, v132, v22
	v_mul_f32_e64 v137, v133, v22
	v_mul_f32_e64 v138, v98, v22
	v_fma_f32 v29, v46, v22, v26
	v_mul_f32_e64 v56, v47, v22
	v_mul_f32_e64 v114, v50, v22
	v_fma_f32 v115, v86, v22, v26
	v_mul_f32_e64 v130, v51, v22
	v_fma_f32 v131, v87, v22, v26
	v_fma_f32 v29, -v136, v136, v29
	v_fma_f32 v56, -v136, v137, v56
	v_fma_f32 v114, -v136, v138, v114
	v_fma_f32 v115, -v137, v137, v115
	v_fma_f32 v130, -v137, v138, v130
	v_fma_f32 v131, -v138, v138, v131
	v_mul_f32_e64 v148, v130, v130
	v_mul_f32_e64 v149, v56, v131
	v_mul_f32_e64 v154, v114, v115
	v_mul_f32_e64 v155, v114, v114
	v_mul_f32_e64 v156, v29, v130
	v_mul_f32_e64 v157, v56, v56
	v_fma_f32 v148, v115, v131, -v148
	v_fma_f32 v149, v114, v130, -v149
	v_fma_f32 v154, v56, v130, -v154
	v_fma_f32 v155, v29, v131, -v155
	v_fma_f32 v156, v56, v114, -v156
	v_fma_f32 v157, v29, v115, -v157
	v_mul_f32_e64 v158, v29, v148
	v_fma_f32 v158, v56, v149, v158
	v_fma_f32 v158, v114, v154, v158
	v_rcp_f32_e32 v158, v158
	v_cmp_ne_u32_e64 vcc, s37, v16
	v_mul_f32_e64 v158, v158, v22
	v_cndmask_b32_e64 v158, 0, v158, s[30:31]
	v_cndmask_b32_e64 v29, 0, v18, vcc
	v_cndmask_b32_e64 v145, 0, v22, s[30:31]
	v_mul_f32_e64 v139, v148, v158
	v_mul_f32_e64 v140, v149, v158
	v_mul_f32_e64 v141, v154, v158
	v_mul_f32_e64 v142, v155, v158
	v_mul_f32_e64 v143, v156, v158
	v_mul_f32_e64 v144, v157, v158
	v_add_f32_e64 v146, v99, v29
	v_mov_b32_e32 v147, v16
	ds_write_b128 v23, v[136:139]
	ds_write_b128 v23, v[140:143] offset:1024
	ds_write_b128 v23, v[144:147] offset:2048
	v_mov_b32_dpp v46, v4 wave_shr:1 row_mask:0xf bank_mask:0xf bound_ctrl:1
	v_mov_b32_dpp v47, v5 wave_shr:1 row_mask:0xf bank_mask:0xf bound_ctrl:1
	v_mov_b32_dpp v50, v4 wave_shl:1 row_mask:0xf bank_mask:0xf bound_ctrl:1
	v_mov_b32_dpp v51, v5 wave_shl:1 row_mask:0xf bank_mask:0xf bound_ctrl:1
	v_pk_mul_f32 v[132:133], v[4:5], v[8:9] op_sel_hi:[1,0]
	v_pk_mul_f32 v[148:149], v[4:5], v[8:9] op_sel:[0,1]
	v_pk_mul_f32 v[156:157], v[4:5], v[10:11] op_sel_hi:[1,0]
	v_pk_add_f32 v[160:161], v[4:5], v[46:47]
	v_pk_fma_f32 v[132:133], v[46:47], v[80:81], v[132:133] op_sel_hi:[1,0,1]
	v_pk_fma_f32 v[148:149], v[46:47], v[80:81], v[148:149] op_sel:[0,1,0]
	v_pk_fma_f32 v[156:157], v[46:47], v[82:83], v[156:157] op_sel_hi:[1,0,1]
	v_pk_add_f32 v[160:161], v[160:161], v[50:51]
	v_pk_fma_f32 v[132:133], v[50:51], v[104:105], v[132:133] op_sel_hi:[1,0,1]
	v_pk_fma_f32 v[148:149], v[50:51], v[104:105], v[148:149] op_sel:[0,1,0]
	v_pk_fma_f32 v[156:157], v[50:51], v[106:107], v[156:157] op_sel_hi:[1,0,1]
	s_waitcnt lgkmcnt(0)
	s_barrier
	v_pk_add_f32 v[46:47], v[150:151], v[160:161]
	v_pk_add_f32 v[50:51], v[152:153], v[46:47]
	v_pk_add_f32 v[86:87], v[38:39], v[132:133]
	v_pk_add_f32 v[152:153], v[64:65], v[86:87]
	v_pk_add_f32 v[38:39], v[122:123], v[148:149]
	v_pk_add_f32 v[64:65], v[84:85], v[38:39]
	v_pk_add_f32 v[98:99], v[134:135], v[156:157]
	v_pk_add_f32 v[84:85], v[116:117], v[98:99]
	v_pk_fma_f32 v[152:153], v[136:137], v[50:51], v[152:153] op_sel_hi:[0,1,1] neg_lo:[1,0,0] neg_hi:[1,0,0]
	v_pk_fma_f32 v[64:65], v[136:137], v[50:51], v[64:65] op_sel:[1,0,0] neg_lo:[1,0,0] neg_hi:[1,0,0]
	v_pk_fma_f32 v[84:85], v[138:139], v[50:51], v[84:85] op_sel_hi:[0,1,1] neg_lo:[1,0,0] neg_hi:[1,0,0]
	v_pk_mul_f32 v[114:115], v[138:139], v[152:153] op_sel:[1,0]
	v_pk_mul_f32 v[122:123], v[140:141], v[152:153] op_sel_hi:[0,1]
	v_pk_mul_f32 v[130:131], v[140:141], v[152:153] op_sel:[1,0]
	v_pk_fma_f32 v[114:115], v[140:141], v[64:65], v[114:115] op_sel_hi:[0,1,1]
	v_pk_fma_f32 v[122:123], v[142:143], v[64:65], v[122:123] op_sel_hi:[0,1,1]
	v_pk_fma_f32 v[130:131], v[142:143], v[64:65], v[130:131] op_sel:[1,0,0]
	v_pk_fma_f32 v[114:115], v[140:141], v[84:85], v[114:115] op_sel:[1,0,0]
	v_pk_fma_f32 v[122:123], v[142:143], v[84:85], v[122:123] op_sel:[1,0,0]
	v_pk_fma_f32 v[130:131], v[144:145], v[84:85], v[130:131] op_sel_hi:[0,1,1]
	v_pk_mul_f32 v[116:117], v[136:137], v[114:115] op_sel_hi:[0,1]
	v_pk_fma_f32 v[116:117], v[136:137], v[122:123], v[116:117] op_sel:[1,0,0]
	v_pk_fma_f32 v[116:117], v[138:139], v[130:131], v[116:117] op_sel_hi:[0,1,1]
	v_pk_fma_f32 v[116:117], v[144:145], v[50:51], v[116:117] op_sel:[1,0,0] neg_lo:[0,0,1] neg_hi:[0,0,1]
	v_cmp_eq_u32_e64 s[10:11], 6, v147
	v_cmp_eq_u32_e64 s[14:15], 7, v147
	v_pk_add_f32 v[64:65], v[48:49], v[114:115]
	v_pk_add_f32 v[50:51], v[54:55], v[64:65]
	v_pk_add_f32 v[48:49], v[92:93], v[122:123]
	v_pk_add_f32 v[54:55], v[58:59], v[48:49]
	v_pk_add_f32 v[84:85], v[96:97], v[130:131]
	v_pk_add_f32 v[58:59], v[66:67], v[84:85]
	v_pk_add_f32 v[66:67], v[166:167], v[116:117]
	v_pk_add_f32 v[92:93], v[128:129], v[66:67]
	v_pk_fma_f32 v[96:97], v[100:101], v[50:51], v[92:93] op_sel_hi:[0,1,1]
	v_pk_fma_f32 v[128:129], v[108:109], v[50:51], v[92:93] op_sel_hi:[0,1,1]
	v_pk_fma_f32 v[96:97], v[100:101], v[54:55], v[96:97] op_sel:[1,0,0]
	v_pk_fma_f32 v[128:129], v[108:109], v[54:55], v[128:129] op_sel:[1,0,0]
	v_pk_fma_f32 v[96:97], v[102:103], v[58:59], v[96:97] op_sel_hi:[0,1,1]
	v_pk_fma_f32 v[128:129], v[110:111], v[58:59], v[128:129] op_sel_hi:[0,1,1]
	v_pk_fma_f32 v[92:93], v[40:41], v[50:51], v[92:93] op_sel_hi:[0,1,1]
	v_pk_fma_f32 v[92:93], v[40:41], v[54:55], v[92:93] op_sel:[1,0,0]
	v_pk_fma_f32 v[92:93], v[42:43], v[58:59], v[92:93] op_sel_hi:[0,1,1]
	v_cndmask_b32_e64 v134, 0, v18, s[10:11]
	v_cndmask_b32_e64 v135, 0, v18, s[14:15]
	v_add_f32_dpp v92, v96, v92 wave_shl:1 row_mask:0xf bank_mask:0xf bound_ctrl:1
	v_add_f32_dpp v93, v97, v93 wave_shl:1 row_mask:0xf bank_mask:0xf bound_ctrl:1
	s_add_i32 s4, s34, 6
	s_cmpk_lt_i32 s4, 0x201
	s_cselect_b64 s[12:13], s[0:1], 0
	v_add_f32_dpp v92, v128, v92 wave_shr:1 row_mask:0xf bank_mask:0xf bound_ctrl:1
	v_add_f32_dpp v93, v129, v93 wave_shr:1 row_mask:0xf bank_mask:0xf bound_ctrl:1
	v_pk_fma_f32 v[92:93], v[36:37], v[146:147], v[92:93] op_sel_hi:[1,0,1] neg_lo:[0,0,1] neg_hi:[0,0,1]
	v_pk_add_f32 v[92:93], v[92:93], v[134:135] neg_lo:[0,1] neg_hi:[0,1]
	v_pk_mul_f32 v[150:151], v[92:93], v[92:93]
	v_add_f32_e32 v150, v150, v151
	v_cndmask_b32_e64 v151, 0, v150, s[12:13]
	v_add_f32_e32 v1, v1, v151
	s_add_i32 s5, s34, 11
	s_min_i32 s5, s5, 0x200
	s_mul_i32 s6, s5, 0x804
	s_add_i32 s6, s6, s35
	s_add_i32 s7, s6, 0x505014
	s_add_i32 s8, s6, 0x606018
	s_mul_i32 s9, s5, 0x180c
	s_add_i32 s9, s9, s33
	s_add_i32 s4, s34, 12
	s_min_i32 s4, s4, 0x200
	s_mul_i32 s4, s4, 0x804
	s_add_i32 s4, s4, s38
	buffer_load_dword v16, v28, s[20:23], s4 offen nt
	buffer_load_dwordx3 v[40:42], v27, s[24:27], s9 offen nt
	buffer_load_dword v36, v28, s[16:19], s7 offen nt
	buffer_load_dword v37, v28, s[16:19], s8 offen nt
	s_waitcnt vmcnt(8)
	v_mov_b32_dpp v100, v12 wave_shr:1 row_mask:0xf bank_mask:0xf bound_ctrl:1
	v_mov_b32_dpp v101, v13 wave_shr:1 row_mask:0xf bank_mask:0xf bound_ctrl:1
	v_mov_b32_dpp v102, v14 wave_shr:1 row_mask:0xf bank_mask:0xf bound_ctrl:1
	v_mov_b32_dpp v108, v12 wave_shl:1 row_mask:0xf bank_mask:0xf bound_ctrl:1
	v_mov_b32_dpp v109, v13 wave_shl:1 row_mask:0xf bank_mask:0xf bound_ctrl:1
	v_mov_b32_dpp v110, v14 wave_shl:1 row_mask:0xf bank_mask:0xf bound_ctrl:1
	s_add_i32 s4, s34, 10
	s_cmpk_lt_u32 s4, 0x201
	s_cselect_b64 s[12:13], s[40:41], 0
	v_cmp_eq_u32_e64 s[14:15], s37, v2
	s_and_b64 s[14:15], s[14:15], s[12:13]
	v_cndmask_b32_e64 v29, 0, 1, s[14:15]
	v_pk_add_f32 v[50:51], v[12:13], v[100:101]
	v_pk_mul_f32 v[54:55], v[12:13], v[12:13] op_sel_hi:[0,1]
	v_or_b32_dpp v56, v29, v29 wave_shr:1 row_mask:0xf bank_mask:0xf bound_ctrl:1
	v_pk_mul_f32 v[58:59], v[12:13], v[14:15] op_sel_hi:[1,0]
	v_or_b32_dpp v56, v29, v56 wave_shl:1 row_mask:0xf bank_mask:0xf bound_ctrl:1
	v_mul_f32_e64 v92, v13, v13
	v_mul_f32_e64 v93, v14, v14
	v_or_b32_dpp v89, v56, v56 wave_shr:1 row_mask:0xf bank_mask:0xf bound_ctrl:1
	v_add_f32_e64 v96, v14, v102
	v_pk_add_f32 v[50:51], v[50:51], v[108:109]
	v_or_b32_dpp v89, v56, v89 wave_shl:1 row_mask:0xf bank_mask:0xf bound_ctrl:1
	v_or3_b32 v29, v89, v118, v119
	v_or3_b32 v29, v29, v57, v88
	s_add_i32 s4, s34, 7
	s_cmpk_lt_u32 s4, 0x1ff
	s_cselect_b64 s[12:13], s[42:43], 0
	v_cmp_ne_u32_e64 s[30:31], 0, v29
	s_and_b64 s[30:31], s[30:31], s[12:13]
	v_cndmask_b32_e64 v29, 0, 1.0, s[30:31]
	v_pk_fma_f32 v[54:55], v[100:101], v[100:101], v[54:55] op_sel_hi:[0,1,1]
	v_pk_fma_f32 v[58:59], v[100:101], v[102:103], v[58:59] op_sel_hi:[1,0,1]
	v_fma_f32 v92, v101, v101, v92
	v_fma_f32 v93, v102, v102, v93
	v_add_f32_dpp v97, v29, v29 wave_shr:1 row_mask:0xf bank_mask:0xf bound_ctrl:1
	v_add_f32_e64 v96, v96, v110
	v_pk_fma_f32 v[54:55], v[108:109], v[108:109], v[54:55] op_sel_hi:[0,1,1]
	v_pk_fma_f32 v[58:59], v[108:109], v[110:111], v[58:59] op_sel_hi:[1,0,1]
	v_fma_f32 v92, v109, v109, v92
	v_fma_f32 v93, v110, v110, v93
	v_add_f32_dpp v97, v29, v97 wave_shl:1 row_mask:0xf bank_mask:0xf bound_ctrl:1
	v_pk_add_f32 v[128:129], v[120:121], v[50:51]
	v_pk_add_f32 v[120:121], v[44:45], v[54:55]
	v_pk_add_f32 v[44:45], v[60:61], v[58:59]
	v_pk_add_f32 v[60:61], v[70:71], v[92:93]
	v_pk_add_f32 v[70:71], v[112:113], v[96:97]
	v_mul_f32_e64 v136, v128, v22
	v_mul_f32_e64 v137, v129, v22
	v_mul_f32_e64 v138, v70, v22
	v_fma_f32 v29, v120, v22, v26
	v_mul_f32_e64 v56, v121, v22
	v_mul_f32_e64 v112, v44, v22
	v_fma_f32 v113, v60, v22, v26
	v_mul_f32_e64 v134, v45, v22
	v_fma_f32 v135, v61, v22, v26
	v_fma_f32 v29, -v136, v136, v29
	v_fma_f32 v56, -v136, v137, v56
	v_fma_f32 v112, -v136, v138, v112
	v_fma_f32 v113, -v137, v137, v113
	v_fma_f32 v134, -v137, v138, v134
	v_fma_f32 v135, -v138, v138, v135
	v_mul_f32_e64 v150, v134, v134
	v_mul_f32_e64 v151, v56, v135
	v_mul_f32_e64 v152, v112, v113
	v_mul_f32_e64 v153, v112, v112
	v_mul_f32_e64 v154, v29, v134
	v_mul_f32_e64 v155, v56, v56
	v_fma_f32 v150, v113, v135, -v150
	v_fma_f32 v151, v112, v134, -v151
	v_fma_f32 v152, v56, v134, -v152
	v_fma_f32 v153, v29, v135, -v153
	v_fma_f32 v154, v56, v112, -v154
	v_fma_f32 v155, v29, v113, -v155
	v_mul_f32_e64 v158, v29, v150
	v_fma_f32 v158, v56, v151, v158
	v_fma_f32 v158, v112, v152, v158
	v_rcp_f32_e32 v158, v158
	v_cmp_ne_u32_e64 vcc, s37, v25
	v_mul_f32_e64 v158, v158, v22
	v_cndmask_b32_e64 v158, 0, v158, s[30:31]
	v_cndmask_b32_e64 v29, 0, v18, vcc
	v_cndmask_b32_e64 v145, 0, v22, s[30:31]
	v_mul_f32_e64 v139, v150, v158
	v_mul_f32_e64 v140, v151, v158
	v_mul_f32_e64 v141, v152, v158
	v_mul_f32_e64 v142, v153, v158
	v_mul_f32_e64 v143, v154, v158
	v_mul_f32_e64 v144, v155, v158
	v_add_f32_e64 v146, v71, v29
	v_mov_b32_e32 v147, v25
	ds_write_b128 v23, v[136:139] offset:3072
	ds_write_b128 v23, v[140:143] offset:4096
	ds_write_b128 v23, v[144:147] offset:5120
	v_mov_b32_dpp v44, v6 wave_shr:1 row_mask:0xf bank_mask:0xf bound_ctrl:1
	v_mov_b32_dpp v45, v7 wave_shr:1 row_mask:0xf bank_mask:0xf bound_ctrl:1
	v_mov_b32_dpp v60, v6 wave_shl:1 row_mask:0xf bank_mask:0xf bound_ctrl:1
	v_mov_b32_dpp v61, v7 wave_shl:1 row_mask:0xf bank_mask:0xf bound_ctrl:1
	v_pk_mul_f32 v[70:71], v[6:7], v[12:13] op_sel_hi:[1,0]
	v_pk_mul_f32 v[134:135], v[6:7], v[12:13] op_sel:[0,1]
	v_pk_mul_f32 v[150:151], v[6:7], v[14:15] op_sel_hi:[1,0]
	v_pk_add_f32 v[154:155], v[6:7], v[44:45]
	v_pk_fma_f32 v[70:71], v[44:45], v[100:101], v[70:71] op_sel_hi:[1,0,1]
	v_pk_fma_f32 v[134:135], v[44:45], v[100:101], v[134:135] op_sel:[0,1,0]
	v_pk_fma_f32 v[150:151], v[44:45], v[102:103], v[150:151] op_sel_hi:[1,0,1]
	v_pk_add_f32 v[154:155], v[154:155], v[60:61]
	v_pk_fma_f32 v[70:71], v[60:61], v[108:109], v[70:71] op_sel_hi:[1,0,1]
	v_pk_fma_f32 v[134:135], v[60:61], v[108:109], v[134:135] op_sel:[0,1,0]
	v_pk_fma_f32 v[150:151], v[60:61], v[110:111], v[150:151] op_sel_hi:[1,0,1]
	s_waitcnt lgkmcnt(0)
	s_barrier
	v_pk_add_f32 v[44:45], v[46:47], v[154:155]
	v_pk_add_f32 v[46:47], v[86:87], v[70:71]
	v_pk_add_f32 v[86:87], v[38:39], v[134:135]
	v_pk_add_f32 v[38:39], v[98:99], v[150:151]
	v_pk_fma_f32 v[46:47], v[136:137], v[44:45], v[46:47] op_sel_hi:[0,1,1] neg_lo:[1,0,0] neg_hi:[1,0,0]
	v_pk_fma_f32 v[86:87], v[136:137], v[44:45], v[86:87] op_sel:[1,0,0] neg_lo:[1,0,0] neg_hi:[1,0,0]
	v_pk_fma_f32 v[38:39], v[138:139], v[44:45], v[38:39] op_sel_hi:[0,1,1] neg_lo:[1,0,0] neg_hi:[1,0,0]
	v_pk_mul_f32 v[60:61], v[138:139], v[46:47] op_sel:[1,0]
	v_pk_mul_f32 v[112:113], v[140:141], v[46:47] op_sel_hi:[0,1]
	v_pk_mul_f32 v[120:121], v[140:141], v[46:47] op_sel:[1,0]
	v_pk_fma_f32 v[60:61], v[140:141], v[86:87], v[60:61] op_sel_hi:[0,1,1]
	v_pk_fma_f32 v[112:113], v[142:143], v[86:87], v[112:113] op_sel_hi:[0,1,1]
	v_pk_fma_f32 v[120:121], v[142:143], v[86:87], v[120:121] op_sel:[1,0,0]
	v_pk_fma_f32 v[60:61], v[140:141], v[38:39], v[60:61] op_sel:[1,0,0]
	v_pk_fma_f32 v[112:113], v[142:143], v[38:39], v[112:113] op_sel:[1,0,0]
	v_pk_fma_f32 v[120:121], v[144:145], v[38:39], v[120:121] op_sel_hi:[0,1,1]
	v_pk_mul_f32 v[98:99], v[136:137], v[60:61] op_sel_hi:[0,1]
	v_pk_fma_f32 v[98:99], v[136:137], v[112:113], v[98:99] op_sel:[1,0,0]
	v_pk_fma_f32 v[98:99], v[138:139], v[120:121], v[98:99] op_sel_hi:[0,1,1]
	v_pk_fma_f32 v[98:99], v[144:145], v[44:45], v[98:99] op_sel:[1,0,0] neg_lo:[0,0,1] neg_hi:[0,0,1]
	v_cmp_eq_u32_e64 s[10:11], 6, v147
	v_cmp_eq_u32_e64 s[14:15], 7, v147
	v_pk_add_f32 v[38:39], v[64:65], v[60:61]
	v_pk_add_f32 v[44:45], v[48:49], v[112:113]
	v_pk_add_f32 v[46:47], v[84:85], v[120:121]
	v_pk_add_f32 v[48:49], v[66:67], v[98:99]
	v_pk_fma_f32 v[64:65], v[72:73], v[38:39], v[48:49] op_sel_hi:[0,1,1]
	v_pk_fma_f32 v[84:85], v[124:125], v[38:39], v[48:49] op_sel_hi:[0,1,1]
	v_pk_fma_f32 v[64:65], v[72:73], v[44:45], v[64:65] op_sel:[1,0,0]
	v_pk_fma_f32 v[84:85], v[124:125], v[44:45], v[84:85] op_sel:[1,0,0]
	v_pk_fma_f32 v[64:65], v[74:75], v[46:47], v[64:65] op_sel_hi:[0,1,1]
	v_pk_fma_f32 v[84:85], v[126:127], v[46:47], v[84:85] op_sel_hi:[0,1,1]
	v_pk_fma_f32 v[48:49], v[76:77], v[38:39], v[48:49] op_sel_hi:[0,1,1]
	v_pk_fma_f32 v[48:49], v[76:77], v[44:45], v[48:49] op_sel:[1,0,0]
	v_pk_fma_f32 v[48:49], v[78:79], v[46:47], v[48:49] op_sel_hi:[0,1,1]
	v_cndmask_b32_e64 v66, 0, v18, s[10:11]
	v_cndmask_b32_e64 v67, 0, v18, s[14:15]
	v_add_f32_dpp v48, v64, v48 wave_shl:1 row_mask:0xf bank_mask:0xf bound_ctrl:1
	v_add_f32_dpp v49, v65, v49 wave_shl:1 row_mask:0xf bank_mask:0xf bound_ctrl:1
	s_add_i32 s4, s34, 7
	s_cmpk_lt_i32 s4, 0x201
	s_cselect_b64 s[12:13], s[0:1], 0
	v_add_f32_dpp v48, v84, v48 wave_shr:1 row_mask:0xf bank_mask:0xf bound_ctrl:1
	v_add_f32_dpp v49, v85, v49 wave_shr:1 row_mask:0xf bank_mask:0xf bound_ctrl:1
	v_pk_fma_f32 v[48:49], v[62:63], v[146:147], v[48:49] op_sel_hi:[1,0,1] neg_lo:[0,0,1] neg_hi:[0,0,1]
	v_pk_add_f32 v[48:49], v[48:49], v[66:67] neg_lo:[0,1] neg_hi:[0,1]
	v_pk_mul_f32 v[86:87], v[48:49], v[48:49]
	v_add_f32_e32 v86, v86, v87
	v_cndmask_b32_e64 v87, 0, v86, s[12:13]
	v_add_f32_e32 v1, v1, v87
	s_waitcnt vmcnt(4)
	v_mov_b32_dpp v44, v32 wave_shr:1 row_mask:0xf bank_mask:0xf bound_ctrl:1
	v_mov_b32_dpp v45, v33 wave_shr:1 row_mask:0xf bank_mask:0xf bound_ctrl:1
	v_mov_b32_dpp v46, v34 wave_shr:1 row_mask:0xf bank_mask:0xf bound_ctrl:1
	v_mov_b32_dpp v64, v32 wave_shl:1 row_mask:0xf bank_mask:0xf bound_ctrl:1
	v_mov_b32_dpp v65, v33 wave_shl:1 row_mask:0xf bank_mask:0xf bound_ctrl:1
	v_mov_b32_dpp v66, v34 wave_shl:1 row_mask:0xf bank_mask:0xf bound_ctrl:1
	s_add_i32 s4, s34, 11
	s_cmpk_lt_u32 s4, 0x201
	s_cselect_b64 s[12:13], s[40:41], 0
	v_cmp_eq_u32_e64 s[14:15], s37, v3
	s_and_b64 s[14:15], s[14:15], s[12:13]
	v_cndmask_b32_e64 v25, 0, 1, s[14:15]
	v_pk_add_f32 v[38:39], v[32:33], v[44:45]
	v_pk_mul_f32 v[48:49], v[32:33], v[32:33] op_sel_hi:[0,1]
	v_or_b32_dpp v29, v25, v25 wave_shr:1 row_mask:0xf bank_mask:0xf bound_ctrl:1
	v_pk_mul_f32 v[62:63], v[32:33], v[34:35] op_sel_hi:[1,0]
	v_or_b32_dpp v29, v25, v29 wave_shl:1 row_mask:0xf bank_mask:0xf bound_ctrl:1
	v_mul_f32_e64 v72, v33, v33
	v_mul_f32_e64 v73, v34, v34
	v_or_b32_dpp v56, v29, v29 wave_shr:1 row_mask:0xf bank_mask:0xf bound_ctrl:1
	v_add_f32_e64 v74, v34, v46
	v_pk_add_f32 v[38:39], v[38:39], v[64:65]
	v_or_b32_dpp v56, v29, v56 wave_shl:1 row_mask:0xf bank_mask:0xf bound_ctrl:1
	v_or3_b32 v25, v56, v89, v118
	v_or3_b32 v25, v25, v119, v57
	s_add_i32 s4, s34, 8
	s_cmpk_lt_u32 s4, 0x1ff
	s_cselect_b64 s[12:13], s[42:43], 0
	v_cmp_ne_u32_e64 s[30:31], 0, v25
	s_and_b64 s[30:31], s[30:31], s[12:13]
	v_cndmask_b32_e64 v25, 0, 1.0, s[30:31]
	v_pk_fma_f32 v[48:49], v[44:45], v[44:45], v[48:49] op_sel_hi:[0,1,1]
	v_pk_fma_f32 v[62:63], v[44:45], v[46:47], v[62:63] op_sel_hi:[1,0,1]
	v_fma_f32 v72, v45, v45, v72
	v_fma_f32 v73, v46, v46, v73
	v_add_f32_dpp v75, v25, v25 wave_shr:1 row_mask:0xf bank_mask:0xf bound_ctrl:1
	v_add_f32_e64 v74, v74, v66
	v_pk_fma_f32 v[48:49], v[64:65], v[64:65], v[48:49] op_sel_hi:[0,1,1]
	v_pk_fma_f32 v[62:63], v[64:65], v[66:67], v[62:63] op_sel_hi:[1,0,1]
	v_fma_f32 v72, v65, v65, v72
	v_fma_f32 v73, v66, v66, v73
	v_add_f32_dpp v75, v25, v75 wave_shl:1 row_mask:0xf bank_mask:0xf bound_ctrl:1
	v_pk_add_f32 v[76:77], v[50:51], v[38:39]
	v_pk_add_f32 v[78:79], v[30:31], v[76:77]
	v_pk_add_f32 v[30:31], v[54:55], v[48:49]
	v_pk_add_f32 v[50:51], v[52:53], v[30:31]
	v_pk_add_f32 v[54:55], v[58:59], v[62:63]
	v_pk_add_f32 v[52:53], v[68:69], v[54:55]
	v_pk_add_f32 v[68:69], v[92:93], v[72:73]
	v_pk_add_f32 v[58:59], v[90:91], v[68:69]
	v_pk_add_f32 v[84:85], v[96:97], v[74:75]
	v_pk_add_f32 v[86:87], v[94:95], v[84:85]
	v_mul_f32_e64 v92, v78, v22
	v_mul_f32_e64 v93, v79, v22
	v_mul_f32_e64 v94, v86, v22
	v_fma_f32 v25, v50, v22, v26
	v_mul_f32_e64 v29, v51, v22
	v_mul_f32_e64 v88, v52, v22
	v_fma_f32 v90, v58, v22, v26
	v_mul_f32_e64 v91, v53, v22
	v_fma_f32 v96, v59, v22, v26
	v_fma_f32 v25, -v92, v92, v25
	v_fma_f32 v29, -v92, v93, v29
	v_fma_f32 v88, -v92, v94, v88
	v_fma_f32 v90, -v93, v93, v90
	v_fma_f32 v91, -v93, v94, v91
	v_fma_f32 v96, -v94, v94, v96
	v_mul_f32_e64 v97, v91, v91
	v_mul_f32_e64 v128, v29, v96
	v_mul_f32_e64 v129, v88, v90
	v_mul_f32_e64 v140, v88, v88
	v_mul_f32_e64 v141, v25, v91
	v_mul_f32_e64 v142, v29, v29
	v_fma_f32 v97, v90, v96, -v97
	v_fma_f32 v128, v88, v91, -v128
	v_fma_f32 v129, v29, v91, -v129
	v_fma_f32 v140, v25, v96, -v140
	v_fma_f32 v141, v29, v88, -v141
	v_fma_f32 v142, v25, v90, -v142
	v_mul_f32_e64 v143, v25, v97
	v_fma_f32 v143, v29, v128, v143
	v_fma_f32 v143, v88, v129, v143
	v_rcp_f32_e32 v143, v143
	v_cmp_ne_u32_e64 vcc, s37, v24
	v_mul_f32_e64 v143, v143, v22
	v_cndmask_b32_e64 v143, 0, v143, s[30:31]
	v_cndmask_b32_e64 v25, 0, v18, vcc
	v_cndmask_b32_e64 v137, 0, v22, s[30:31]
	v_mul_f32_e64 v95, v97, v143
	v_mul_f32_e64 v124, v128, v143
	v_mul_f32_e64 v125, v129, v143
	v_mul_f32_e64 v126, v140, v143
	v_mul_f32_e64 v127, v141, v143
	v_mul_f32_e64 v136, v142, v143
	v_add_f32_e64 v138, v87, v25
	v_mov_b32_e32 v139, v24
	ds_write_b128 v23, v[92:95]
	ds_write_b128 v23, v[124:127] offset:1024
	ds_write_b128 v23, v[136:139] offset:2048
	v_mov_b32_dpp v50, v20 wave_shr:1 row_mask:0xf bank_mask:0xf bound_ctrl:1
	v_mov_b32_dpp v51, v21 wave_shr:1 row_mask:0xf bank_mask:0xf bound_ctrl:1
	v_mov_b32_dpp v58, v20 wave_shl:1 row_mask:0xf bank_mask:0xf bound_ctrl:1
	v_mov_b32_dpp v59, v21 wave_shl:1 row_mask:0xf bank_mask:0xf bound_ctrl:1
	v_pk_mul_f32 v[24:25], v[20:21], v[32:33] op_sel_hi:[1,0]
	v_pk_mul_f32 v[52:53], v[20:21], v[32:33] op_sel:[0,1]
	v_pk_mul_f32 v[96:97], v[20:21], v[34:35] op_sel_hi:[1,0]
	v_pk_add_f32 v[128:129], v[20:21], v[50:51]
	v_pk_fma_f32 v[24:25], v[50:51], v[44:45], v[24:25] op_sel_hi:[1,0,1]
	v_pk_fma_f32 v[52:53], v[50:51], v[44:45], v[52:53] op_sel:[0,1,0]
	v_pk_fma_f32 v[96:97], v[50:51], v[46:47], v[96:97] op_sel_hi:[1,0,1]
	v_pk_add_f32 v[128:129], v[128:129], v[58:59]
	v_pk_fma_f32 v[24:25], v[58:59], v[64:65], v[24:25] op_sel_hi:[1,0,1]
	v_pk_fma_f32 v[52:53], v[58:59], v[64:65], v[52:53] op_sel:[0,1,0]
	v_pk_fma_f32 v[96:97], v[58:59], v[66:67], v[96:97] op_sel_hi:[1,0,1]
	s_waitcnt lgkmcnt(0)
	s_barrier
	v_pk_add_f32 v[50:51], v[154:155], v[128:129]
	v_pk_add_f32 v[58:59], v[160:161], v[50:51]
	v_pk_add_f32 v[78:79], v[70:71], v[24:25]
	v_pk_add_f32 v[140:141], v[132:133], v[78:79]
	v_pk_add_f32 v[70:71], v[134:135], v[52:53]
	v_pk_add_f32 v[132:133], v[148:149], v[70:71]
	v_pk_add_f32 v[86:87], v[150:151], v[96:97]
	v_pk_add_f32 v[144:145], v[156:157], v[86:87]
	v_pk_fma_f32 v[140:141], v[92:93], v[58:59], v[140:141] op_sel_hi:[0,1,1] neg_lo:[1,0,0] neg_hi:[1,0,0]
	v_pk_fma_f32 v[132:133], v[92:93], v[58:59], v[132:133] op_sel:[1,0,0] neg_lo:[1,0,0] neg_hi:[1,0,0]
	v_pk_fma_f32 v[144:145], v[94:95], v[58:59], v[144:145] op_sel_hi:[0,1,1] neg_lo:[1,0,0] neg_hi:[1,0,0]
	v_pk_mul_f32 v[90:91], v[94:95], v[140:141] op_sel:[1,0]
	v_pk_mul_f32 v[134:135], v[124:125], v[140:141] op_sel_hi:[0,1]
	v_pk_mul_f32 v[142:143], v[124:125], v[140:141] op_sel:[1,0]
	v_pk_fma_f32 v[90:91], v[124:125], v[132:133], v[90:91] op_sel_hi:[0,1,1]
	v_pk_fma_f32 v[134:135], v[126:127], v[132:133], v[134:135] op_sel_hi:[0,1,1]
	v_pk_fma_f32 v[142:143], v[126:127], v[132:133], v[142:143] op_sel:[1,0,0]
	v_pk_fma_f32 v[90:91], v[124:125], v[144:145], v[90:91] op_sel:[1,0,0]
	v_pk_fma_f32 v[134:135], v[126:127], v[144:145], v[134:135] op_sel:[1,0,0]
	v_pk_fma_f32 v[142:143], v[136:137], v[144:145], v[142:143] op_sel_hi:[0,1,1]
	v_pk_mul_f32 v[148:149], v[92:93], v[90:91] op_sel_hi:[0,1]
	v_pk_fma_f32 v[148:149], v[92:93], v[134:135], v[148:149] op_sel:[1,0,0]
	v_pk_fma_f32 v[148:149], v[94:95], v[142:143], v[148:149] op_sel_hi:[0,1,1]
	v_pk_fma_f32 v[148:149], v[136:137], v[58:59], v[148:149] op_sel:[1,0,0] neg_lo:[0,0,1] neg_hi:[0,0,1]
	v_cmp_eq_u32_e64 s[10:11], 6, v139
	v_cmp_eq_u32_e64 s[14:15], 7, v139
	v_pk_add_f32 v[132:133], v[60:61], v[90:91]
	v_pk_add_f32 v[58:59], v[114:115], v[132:133]
	v_pk_add_f32 v[60:61], v[112:113], v[134:135]
	v_pk_add_f32 v[114:115], v[122:123], v[60:61]
	v_pk_add_f32 v[112:113], v[120:121], v[142:143]
	v_pk_add_f32 v[122:123], v[130:131], v[112:113]
	v_pk_add_f32 v[130:131], v[98:99], v[148:149]
	v_pk_add_f32 v[120:121], v[116:117], v[130:131]
	v_pk_fma_f32 v[116:117], v[80:81], v[58:59], v[120:121] op_sel_hi:[0,1,1]
	v_pk_fma_f32 v[140:141], v[104:105], v[58:59], v[120:121] op_sel_hi:[0,1,1]
	v_pk_fma_f32 v[116:117], v[80:81], v[114:115], v[116:117] op_sel:[1,0,0]
	v_pk_fma_f32 v[140:141], v[104:105], v[114:115], v[140:141] op_sel:[1,0,0]
	v_pk_fma_f32 v[116:117], v[82:83], v[122:123], v[116:117] op_sel_hi:[0,1,1]
	v_pk_fma_f32 v[140:141], v[106:107], v[122:123], v[140:141] op_sel_hi:[0,1,1]
	v_pk_fma_f32 v[120:121], v[8:9], v[58:59], v[120:121] op_sel_hi:[0,1,1]
	v_pk_fma_f32 v[120:121], v[8:9], v[114:115], v[120:121] op_sel:[1,0,0]
	v_pk_fma_f32 v[120:121], v[10:11], v[122:123], v[120:121] op_sel_hi:[0,1,1]
	v_cndmask_b32_e64 v98, 0, v18, s[10:11]
	v_cndmask_b32_e64 v99, 0, v18, s[14:15]
	v_add_f32_dpp v120, v116, v120 wave_shl:1 row_mask:0xf bank_mask:0xf bound_ctrl:1
	v_add_f32_dpp v121, v117, v121 wave_shl:1 row_mask:0xf bank_mask:0xf bound_ctrl:1
	s_add_i32 s4, s34, 8
	s_cmpk_lt_i32 s4, 0x201
	s_cselect_b64 s[12:13], s[0:1], 0
	v_add_f32_dpp v120, v140, v120 wave_shr:1 row_mask:0xf bank_mask:0xf bound_ctrl:1
	v_add_f32_dpp v121, v141, v121 wave_shr:1 row_mask:0xf bank_mask:0xf bound_ctrl:1
	v_pk_fma_f32 v[120:121], v[4:5], v[138:139], v[120:121] op_sel_hi:[1,0,1] neg_lo:[0,0,1] neg_hi:[0,0,1]
	v_pk_add_f32 v[120:121], v[120:121], v[98:99] neg_lo:[0,1] neg_hi:[0,1]
	v_pk_mul_f32 v[144:145], v[120:121], v[120:121]
	v_add_f32_e32 v144, v144, v145
	v_cndmask_b32_e64 v145, 0, v144, s[12:13]
	v_add_f32_e32 v1, v1, v145
	s_waitcnt vmcnt(0)
	v_mov_b32_dpp v8, v40 wave_shr:1 row_mask:0xf bank_mask:0xf bound_ctrl:1
	v_mov_b32_dpp v9, v41 wave_shr:1 row_mask:0xf bank_mask:0xf bound_ctrl:1
	v_mov_b32_dpp v10, v42 wave_shr:1 row_mask:0xf bank_mask:0xf bound_ctrl:1
	v_mov_b32_dpp v80, v40 wave_shl:1 row_mask:0xf bank_mask:0xf bound_ctrl:1
	v_mov_b32_dpp v81, v41 wave_shl:1 row_mask:0xf bank_mask:0xf bound_ctrl:1
	v_mov_b32_dpp v82, v42 wave_shl:1 row_mask:0xf bank_mask:0xf bound_ctrl:1
	s_add_i32 s4, s34, 12
	s_cmpk_lt_u32 s4, 0x201
	s_cselect_b64 s[12:13], s[40:41], 0
	v_cmp_eq_u32_e64 s[14:15], s37, v16
	s_and_b64 s[14:15], s[14:15], s[12:13]
	v_cndmask_b32_e64 v29, 0, 1, s[14:15]
	v_pk_add_f32 v[4:5], v[40:41], v[8:9]
	v_pk_mul_f32 v[58:59], v[40:41], v[40:41] op_sel_hi:[0,1]
	v_or_b32_dpp v57, v29, v29 wave_shr:1 row_mask:0xf bank_mask:0xf bound_ctrl:1
	v_pk_mul_f32 v[92:93], v[40:41], v[42:43] op_sel_hi:[1,0]
	v_or_b32_dpp v57, v29, v57 wave_shl:1 row_mask:0xf bank_mask:0xf bound_ctrl:1
	v_mul_f32_e64 v94, v41, v41
	v_mul_f32_e64 v95, v42, v42
	v_or_b32_dpp v88, v57, v57 wave_shr:1 row_mask:0xf bank_mask:0xf bound_ctrl:1
	v_add_f32_e64 v98, v42, v10
	v_pk_add_f32 v[4:5], v[4:5], v[80:81]
	v_or_b32_dpp v88, v57, v88 wave_shl:1 row_mask:0xf bank_mask:0xf bound_ctrl:1
	v_or3_b32 v29, v88, v56, v89
	v_or3_b32 v29, v29, v118, v119
	s_add_i32 s4, s34, 9
	s_cmpk_lt_u32 s4, 0x1ff
	s_cselect_b64 s[12:13], s[42:43], 0
	v_cmp_ne_u32_e64 s[30:31], 0, v29
	s_and_b64 s[30:31], s[30:31], s[12:13]
	v_cndmask_b32_e64 v29, 0, 1.0, s[30:31]
	v_pk_fma_f32 v[58:59], v[8:9], v[8:9], v[58:59] op_sel_hi:[0,1,1]
	v_pk_fma_f32 v[92:93], v[8:9], v[10:11], v[92:93] op_sel_hi:[1,0,1]
	v_fma_f32 v94, v9, v9, v94
	v_fma_f32 v95, v10, v10, v95
	v_add_f32_dpp v99, v29, v29 wave_shr:1 row_mask:0xf bank_mask:0xf bound_ctrl:1
	v_add_f32_e64 v98, v98, v82
	v_pk_fma_f32 v[58:59], v[80:81], v[80:81], v[58:59] op_sel_hi:[0,1,1]
	v_pk_fma_f32 v[92:93], v[80:81], v[82:83], v[92:93] op_sel_hi:[1,0,1]
	v_fma_f32 v94, v81, v81, v94
	v_fma_f32 v95, v82, v82, v95
	v_add_f32_dpp v99, v29, v99 wave_shl:1 row_mask:0xf bank_mask:0xf bound_ctrl:1
	v_pk_add_f32 v[104:105], v[76:77], v[4:5]
	v_pk_add_f32 v[76:77], v[30:31], v[58:59]
	v_pk_add_f32 v[30:31], v[54:55], v[92:93]
	v_pk_add_f32 v[54:55], v[68:69], v[94:95]
	v_pk_add_f32 v[68:69], v[84:85], v[98:99]
	v_mul_f32_e64 v120, v104, v22
	v_mul_f32_e64 v121, v105, v22
	v_mul_f32_e64 v122, v68, v22
	v_fma_f32 v29, v76, v22, v26
	v_mul_f32_e64 v57, v77, v22
	v_mul_f32_e64 v84, v30, v22
	v_fma_f32 v85, v54, v22, v26
	v_mul_f32_e64 v106, v31, v22
	v_fma_f32 v107, v55, v22, v26
	v_fma_f32 v29, -v120, v120, v29
	v_fma_f32 v57, -v120, v121, v57
	v_fma_f32 v84, -v120, v122, v84
	v_fma_f32 v85, -v121, v121, v85
	v_fma_f32 v106, -v121, v122, v106
	v_fma_f32 v107, -v122, v122, v107
	v_mul_f32_e64 v114, v106, v106
	v_mul_f32_e64 v115, v57, v107
	v_mul_f32_e64 v116, v84, v85
	v_mul_f32_e64 v117, v84, v84
	v_mul_f32_e64 v140, v29, v106
	v_mul_f32_e64 v141, v57, v57
	v_fma_f32 v114, v85, v107, -v114
	v_fma_f32 v115, v84, v106, -v115
	v_fma_f32 v116, v57, v106, -v116
	v_fma_f32 v117, v29, v107, -v117
	v_fma_f32 v140, v57, v84, -v140
	v_fma_f32 v141, v29, v85, -v141
	v_mul_f32_e64 v144, v29, v114
	v_fma_f32 v144, v57, v115, v144
	v_fma_f32 v144, v84, v116, v144
	v_rcp_f32_e32 v144, v144
	v_cmp_ne_u32_e64 vcc, s37, v17
	v_mul_f32_e64 v144, v144, v22
	v_cndmask_b32_e64 v144, 0, v144, s[30:31]
	v_cndmask_b32_e64 v29, 0, v18, vcc
	v_cndmask_b32_e64 v137, 0, v22, s[30:31]
	v_mul_f32_e64 v123, v114, v144
	v_mul_f32_e64 v124, v115, v144
	v_mul_f32_e64 v125, v116, v144
	v_mul_f32_e64 v126, v117, v144
	v_mul_f32_e64 v127, v140, v144
	v_mul_f32_e64 v136, v141, v144
	v_add_f32_e64 v138, v69, v29
	v_mov_b32_e32 v139, v17
	ds_write_b128 v23, v[120:123] offset:3072
	ds_write_b128 v23, v[124:127] offset:4096
	ds_write_b128 v23, v[136:139] offset:5120
	v_mov_b32_dpp v30, v36 wave_shr:1 row_mask:0xf bank_mask:0xf bound_ctrl:1
	v_mov_b32_dpp v31, v37 wave_shr:1 row_mask:0xf bank_mask:0xf bound_ctrl:1
	v_mov_b32_dpp v54, v36 wave_shl:1 row_mask:0xf bank_mask:0xf bound_ctrl:1
	v_mov_b32_dpp v55, v37 wave_shl:1 row_mask:0xf bank_mask:0xf bound_ctrl:1
	v_pk_mul_f32 v[68:69], v[36:37], v[40:41] op_sel_hi:[1,0]
	v_pk_mul_f32 v[76:77], v[36:37], v[40:41] op_sel:[0,1]
	v_pk_mul_f32 v[84:85], v[36:37], v[42:43] op_sel_hi:[1,0]
	v_pk_add_f32 v[104:105], v[36:37], v[30:31]
	v_pk_fma_f32 v[68:69], v[30:31], v[8:9], v[68:69] op_sel_hi:[1,0,1]
	v_pk_fma_f32 v[76:77], v[30:31], v[8:9], v[76:77] op_sel:[0,1,0]
	v_pk_fma_f32 v[84:85], v[30:31], v[10:11], v[84:85] op_sel_hi:[1,0,1]
	v_pk_add_f32 v[104:105], v[104:105], v[54:55]
	v_pk_fma_f32 v[68:69], v[54:55], v[80:81], v[68:69] op_sel_hi:[1,0,1]
	v_pk_fma_f32 v[76:77], v[54:55], v[80:81], v[76:77] op_sel:[0,1,0]
	v_pk_fma_f32 v[84:85], v[54:55], v[82:83], v[84:85] op_sel_hi:[1,0,1]
	s_waitcnt lgkmcnt(0)
	s_barrier
	v_pk_add_f32 v[30:31], v[50:51], v[104:105]
	v_pk_add_f32 v[116:117], v[78:79], v[68:69]
	v_pk_add_f32 v[140:141], v[70:71], v[76:77]
	v_pk_add_f32 v[144:145], v[86:87], v[84:85]
	v_pk_fma_f32 v[116:117], v[120:121], v[30:31], v[116:117] op_sel_hi:[0,1,1] neg_lo:[1,0,0] neg_hi:[1,0,0]
	v_pk_fma_f32 v[140:141], v[120:121], v[30:31], v[140:141] op_sel:[1,0,0] neg_lo:[1,0,0] neg_hi:[1,0,0]
	v_pk_fma_f32 v[144:145], v[122:123], v[30:31], v[144:145] op_sel_hi:[0,1,1] neg_lo:[1,0,0] neg_hi:[1,0,0]
	v_pk_mul_f32 v[50:51], v[122:123], v[116:117] op_sel:[1,0]
	v_pk_mul_f32 v[54:55], v[124:125], v[116:117] op_sel_hi:[0,1]
	v_pk_mul_f32 v[70:71], v[124:125], v[116:117] op_sel:[1,0]
	v_pk_fma_f32 v[50:51], v[124:125], v[140:141], v[50:51] op_sel_hi:[0,1,1]
	v_pk_fma_f32 v[54:55], v[126:127], v[140:141], v[54:55] op_sel_hi:[0,1,1]
	v_pk_fma_f32 v[70:71], v[126:127], v[140:141], v[70:71] op_sel:[1,0,0]
	v_pk_fma_f32 v[50:51], v[124:125], v[144:145], v[50:51] op_sel:[1,0,0]
	v_pk_fma_f32 v[54:55], v[126:127], v[144:145], v[54:55] op_sel:[1,0,0]
	v_pk_fma_f32 v[70:71], v[136:137], v[144:145], v[70:71] op_sel_hi:[0,1,1]
	v_pk_mul_f32 v[152:153], v[120:121], v[50:51] op_sel_hi:[0,1]
	v_pk_fma_f32 v[152:153], v[120:121], v[54:55], v[152:153] op_sel:[1,0,0]
	v_pk_fma_f32 v[152:153], v[122:123], v[70:71], v[152:153] op_sel_hi:[0,1,1]
	v_pk_fma_f32 v[152:153], v[136:137], v[30:31], v[152:153] op_sel:[1,0,0] neg_lo:[0,0,1] neg_hi:[0,0,1]
	v_cmp_eq_u32_e64 s[10:11], 6, v139
	v_cmp_eq_u32_e64 s[14:15], 7, v139
	v_pk_add_f32 v[30:31], v[132:133], v[50:51]
	v_pk_add_f32 v[78:79], v[60:61], v[54:55]
	v_pk_add_f32 v[60:61], v[112:113], v[70:71]
	v_pk_add_f32 v[112:113], v[130:131], v[152:153]
	v_pk_fma_f32 v[116:117], v[100:101], v[30:31], v[112:113] op_sel_hi:[0,1,1]
	v_pk_fma_f32 v[132:133], v[108:109], v[30:31], v[112:113] op_sel_hi:[0,1,1]
	v_pk_fma_f32 v[116:117], v[100:101], v[78:79], v[116:117] op_sel:[1,0,0]
	v_pk_fma_f32 v[132:133], v[108:109], v[78:79], v[132:133] op_sel:[1,0,0]
	v_pk_fma_f32 v[116:117], v[102:103], v[60:61], v[116:117] op_sel_hi:[0,1,1]
	v_pk_fma_f32 v[132:133], v[110:111], v[60:61], v[132:133] op_sel_hi:[0,1,1]
	v_pk_fma_f32 v[112:113], v[12:13], v[30:31], v[112:113] op_sel_hi:[0,1,1]
	v_pk_fma_f32 v[112:113], v[12:13], v[78:79], v[112:113] op_sel:[1,0,0]
	v_pk_fma_f32 v[112:113], v[14:15], v[60:61], v[112:113] op_sel_hi:[0,1,1]
	v_cndmask_b32_e64 v86, 0, v18, s[10:11]
	v_cndmask_b32_e64 v87, 0, v18, s[14:15]
	v_add_f32_dpp v112, v116, v112 wave_shl:1 row_mask:0xf bank_mask:0xf bound_ctrl:1
	v_add_f32_dpp v113, v117, v113 wave_shl:1 row_mask:0xf bank_mask:0xf bound_ctrl:1
	s_add_i32 s4, s34, 9
	s_cmpk_lt_i32 s4, 0x201
	s_cselect_b64 s[12:13], s[0:1], 0
	v_add_f32_dpp v112, v132, v112 wave_shr:1 row_mask:0xf bank_mask:0xf bound_ctrl:1
	v_add_f32_dpp v113, v133, v113 wave_shr:1 row_mask:0xf bank_mask:0xf bound_ctrl:1
	v_pk_fma_f32 v[112:113], v[6:7], v[138:139], v[112:113] op_sel_hi:[1,0,1] neg_lo:[0,0,1] neg_hi:[0,0,1]
	v_pk_add_f32 v[112:113], v[112:113], v[86:87] neg_lo:[0,1] neg_hi:[0,1]
	v_pk_mul_f32 v[106:107], v[112:113], v[112:113]
	v_add_f32_e32 v106, v106, v107
	v_cndmask_b32_e64 v107, 0, v106, s[12:13]
	v_add_f32_e32 v1, v1, v107
	v_mov_b32_e32 v0, v1
	s_branch .LBB0_29
